# GEMM tile loops keep the two-group ping-pong stagger across tile boundaries: exit barrier only on a nest's last tile, entry barrier between tiles removed (6 nests), on top of v63
# baseline (speedup 1.0000x reference)
.Lmy_peel339_exit:
	s_cmp_lg_u32 s43, s42
	s_cbranch_scc1 .LBB0_344
	s_and_b64 vcc, exec, s[10:11]
	s_cbranch_vccz .LBB0_344
	s_barrier
	v_lshl_add_u32 v134, s78, 8, v140
	s_cmp_gt_i32 s47, 53
	s_mov_b64 s[20:21], -1
	s_cbranch_scc1 .LBB0_345

.LBB0_348:
	s_andn2_b64 vcc, exec, s[2:3]
	s_branch .LBB0_334

.Lmy_peel370_exit:
	s_cmp_lg_u32 s40, s36
	s_cbranch_scc1 .LBB0_373
	s_and_b64 vcc, exec, s[8:9]
	s_cbranch_vccz .LBB0_373
	s_barrier
.LBB0_373:
	v_pk_mul_f32 v[122:123], v[122:123], s[58:59] op_sel_hi:[1,0]
	v_pk_mul_f32 v[126:127], v[126:127], s[58:59] op_sel_hi:[1,0]
	v_mul_f32_e32 v122, 0xbfb8aa3b, v122
	v_exp_f32_e32 v122, v122
	v_mul_f32_e32 v127, 0xbfb8aa3b, v127
	v_exp_f32_e32 v127, v127
	v_pk_mul_f32 v[128:129], v[128:129], s[58:59] op_sel_hi:[1,0]
	v_add_f32_e32 v122, 1.0, v122
	v_mul_f32_e32 v123, 0xbfb8aa3b, v123
	v_exp_f32_e32 v123, v123
	v_rcp_f32_e32 v141, v122
	v_add_f32_e32 v122, 1.0, v127
	v_mul_f32_e32 v127, 0xbfb8aa3b, v128
	v_exp_f32_e32 v127, v127
	v_pk_mul_f32 v[124:125], v[124:125], s[58:59] op_sel_hi:[1,0]
	v_add_f32_e32 v123, 1.0, v123
	v_mul_f32_e32 v124, 0xbfb8aa3b, v124
	v_mul_f32_e32 v126, 0xbfb8aa3b, v126
	v_exp_f32_e32 v124, v124
	v_rcp_f32_e32 v128, v123
	v_add_f32_e32 v123, 1.0, v127
	v_mul_f32_e32 v127, 0xbfb8aa3b, v129
	v_mul_f32_e32 v125, 0xbfb8aa3b, v125
	v_exp_f32_e32 v126, v126
	v_exp_f32_e32 v127, v127
	v_exp_f32_e32 v125, v125
	v_add_f32_e32 v124, 1.0, v124
	v_pk_mul_f32 v[114:115], v[114:115], s[58:59] op_sel_hi:[1,0]
	s_lshl_b32 s16, s41, 8
	v_add_f32_e32 v126, 1.0, v126
	v_rcp_f32_e32 v129, v124
	v_add_f32_e32 v124, 1.0, v127
	v_add_f32_e32 v125, 1.0, v125
	v_pk_mul_f32 v[118:119], v[118:119], s[58:59] op_sel_hi:[1,0]
	v_mul_f32_e32 v114, 0xbfb8aa3b, v114
	v_lshl_add_u32 v96, s42, 8, v138
	s_ashr_i32 s17, s16, 31
	v_mov_b64_e32 v[132:133], s[6:7]
	v_rcp_f32_e32 v126, v126
	v_rcp_f32_e32 v122, v122
	v_rcp_f32_e32 v123, v123
	v_rcp_f32_e32 v124, v124
	v_rcp_f32_e32 v125, v125
	v_exp_f32_e32 v114, v114
	v_mul_f32_e32 v119, 0xbfb8aa3b, v119
	v_mad_i64_i32 v[130:131], s[18:19], v96, s59, v[132:133]
	s_lshl_b64 s[16:17], s[16:17], 1
	v_exp_f32_e32 v119, v119
	v_lshl_add_u64 v[130:131], v[130:131], 0, s[16:17]
	v_lshl_add_u64 v[130:131], v[130:131], 0, s[76:77]
	v_mov_b32_e32 v207, v97
	v_lshl_add_u64 v[130:131], v[130:131], 0, v[206:207]
	v_cvt_pk_bf16_f32 v122, v126, v122
	v_cvt_pk_bf16_f32 v123, v123, v124
	v_cvt_pk_bf16_f32 v124, v141, v128
	v_cvt_pk_bf16_f32 v125, v129, v125
	v_pk_mul_f32 v[120:121], v[120:121], s[58:59] op_sel_hi:[1,0]
	v_add_f32_e32 v114, 1.0, v114
	v_mul_f32_e32 v115, 0xbfb8aa3b, v115
	global_store_dwordx4 v[130:131], v[122:125], off
	v_exp_f32_e32 v115, v115
	v_pk_mul_f32 v[116:117], v[116:117], s[58:59] op_sel_hi:[1,0]
	v_rcp_f32_e32 v122, v114
	v_add_f32_e32 v114, 1.0, v119
	v_mul_f32_e32 v119, 0xbfb8aa3b, v120
	v_exp_f32_e32 v119, v119
	v_add_f32_e32 v115, 1.0, v115
	v_mul_f32_e32 v116, 0xbfb8aa3b, v116
	v_mul_f32_e32 v118, 0xbfb8aa3b, v118
	v_exp_f32_e32 v116, v116
	v_rcp_f32_e32 v120, v115
	v_add_f32_e32 v115, 1.0, v119
	v_mul_f32_e32 v119, 0xbfb8aa3b, v121
	v_mul_f32_e32 v117, 0xbfb8aa3b, v117
	v_exp_f32_e32 v118, v118
	v_exp_f32_e32 v119, v119
	v_exp_f32_e32 v117, v117
	v_add_f32_e32 v116, 1.0, v116
	v_pk_mul_f32 v[106:107], v[106:107], s[58:59] op_sel_hi:[1,0]
	v_add_f32_e32 v118, 1.0, v118
	v_rcp_f32_e32 v121, v116
	v_add_f32_e32 v116, 1.0, v119
	v_add_f32_e32 v117, 1.0, v117
	v_pk_mul_f32 v[110:111], v[110:111], s[58:59] op_sel_hi:[1,0]
	v_mul_f32_e32 v106, 0xbfb8aa3b, v106
	v_rcp_f32_e32 v118, v118
	v_rcp_f32_e32 v114, v114
	v_rcp_f32_e32 v115, v115
	v_rcp_f32_e32 v116, v116
	v_rcp_f32_e32 v117, v117
	v_exp_f32_e32 v106, v106
	v_mul_f32_e32 v111, 0xbfb8aa3b, v111
	v_exp_f32_e32 v111, v111
	v_cvt_pk_bf16_f32 v114, v118, v114
	v_cvt_pk_bf16_f32 v115, v115, v116
	v_cvt_pk_bf16_f32 v116, v122, v120
	v_cvt_pk_bf16_f32 v117, v121, v117
	v_pk_mul_f32 v[112:113], v[112:113], s[58:59] op_sel_hi:[1,0]
	v_add_f32_e32 v106, 1.0, v106
	v_mul_f32_e32 v107, 0xbfb8aa3b, v107
	global_store_dwordx4 v[130:131], v[114:117], off offset:256
	v_exp_f32_e32 v107, v107
	v_pk_mul_f32 v[108:109], v[108:109], s[58:59] op_sel_hi:[1,0]
	v_rcp_f32_e32 v116, v106
	v_add_f32_e32 v106, 1.0, v111
	v_mul_f32_e32 v111, 0xbfb8aa3b, v112
	v_exp_f32_e32 v111, v111
	v_add_f32_e32 v107, 1.0, v107
	v_mul_f32_e32 v108, 0xbfb8aa3b, v108
	v_mul_f32_e32 v110, 0xbfb8aa3b, v110
	v_exp_f32_e32 v108, v108
	v_rcp_f32_e32 v112, v107
	v_add_f32_e32 v107, 1.0, v111
	v_mul_f32_e32 v111, 0xbfb8aa3b, v113
	v_mul_f32_e32 v109, 0xbfb8aa3b, v109
	v_exp_f32_e32 v110, v110
	v_exp_f32_e32 v111, v111
	v_exp_f32_e32 v109, v109
	v_add_f32_e32 v108, 1.0, v108
	v_pk_mul_f32 v[98:99], v[98:99], s[58:59] op_sel_hi:[1,0]
	v_add_f32_e32 v110, 1.0, v110
	v_rcp_f32_e32 v113, v108
	v_add_f32_e32 v108, 1.0, v111
	v_add_f32_e32 v109, 1.0, v109
	v_pk_mul_f32 v[102:103], v[102:103], s[58:59] op_sel_hi:[1,0]
	v_mul_f32_e32 v98, 0xbfb8aa3b, v98
	v_or_b32_e32 v114, 16, v96
	v_rcp_f32_e32 v110, v110
	v_rcp_f32_e32 v106, v106
	v_rcp_f32_e32 v107, v107
	v_rcp_f32_e32 v108, v108
	v_rcp_f32_e32 v109, v109
	v_exp_f32_e32 v98, v98
	v_mul_f32_e32 v103, 0xbfb8aa3b, v103
	v_mad_i64_i32 v[114:115], s[18:19], v114, s59, v[132:133]
	v_exp_f32_e32 v103, v103
	v_lshl_add_u64 v[114:115], v[114:115], 0, s[16:17]
	v_lshl_add_u64 v[114:115], v[114:115], 0, s[76:77]
	v_lshl_add_u64 v[114:115], v[114:115], 0, v[206:207]
	v_cvt_pk_bf16_f32 v106, v110, v106
	v_cvt_pk_bf16_f32 v107, v107, v108
	v_cvt_pk_bf16_f32 v108, v116, v112
	v_cvt_pk_bf16_f32 v109, v113, v109
	v_pk_mul_f32 v[104:105], v[104:105], s[58:59] op_sel_hi:[1,0]
	v_add_f32_e32 v98, 1.0, v98
	v_mul_f32_e32 v99, 0xbfb8aa3b, v99
	global_store_dwordx4 v[114:115], v[106:109], off
	v_exp_f32_e32 v99, v99
	v_pk_mul_f32 v[100:101], v[100:101], s[58:59] op_sel_hi:[1,0]
	v_rcp_f32_e32 v106, v98
	v_add_f32_e32 v98, 1.0, v103
	v_mul_f32_e32 v103, 0xbfb8aa3b, v104
	v_exp_f32_e32 v103, v103
	v_add_f32_e32 v99, 1.0, v99
	v_mul_f32_e32 v100, 0xbfb8aa3b, v100
	v_mul_f32_e32 v102, 0xbfb8aa3b, v102
	v_exp_f32_e32 v100, v100
	v_rcp_f32_e32 v104, v99
	v_add_f32_e32 v99, 1.0, v103
	v_mul_f32_e32 v103, 0xbfb8aa3b, v105
	v_mul_f32_e32 v101, 0xbfb8aa3b, v101
	v_exp_f32_e32 v102, v102
	v_exp_f32_e32 v103, v103
	v_exp_f32_e32 v101, v101
	v_add_f32_e32 v100, 1.0, v100
	v_pk_mul_f32 v[88:89], v[88:89], s[58:59] op_sel_hi:[1,0]
	v_add_f32_e32 v102, 1.0, v102
	v_rcp_f32_e32 v105, v100
	v_add_f32_e32 v100, 1.0, v103
	v_add_f32_e32 v101, 1.0, v101
	v_pk_mul_f32 v[92:93], v[92:93], s[58:59] op_sel_hi:[1,0]
	v_mul_f32_e32 v88, 0xbfb8aa3b, v88
	v_rcp_f32_e32 v102, v102
	v_rcp_f32_e32 v98, v98
	v_rcp_f32_e32 v99, v99
	v_rcp_f32_e32 v100, v100
	v_rcp_f32_e32 v101, v101
	v_exp_f32_e32 v88, v88
	v_mul_f32_e32 v93, 0xbfb8aa3b, v93
	v_exp_f32_e32 v93, v93
	v_cvt_pk_bf16_f32 v98, v102, v98
	v_cvt_pk_bf16_f32 v99, v99, v100
	v_cvt_pk_bf16_f32 v100, v106, v104
	v_cvt_pk_bf16_f32 v101, v105, v101
	v_pk_mul_f32 v[94:95], v[94:95], s[58:59] op_sel_hi:[1,0]
	v_add_f32_e32 v88, 1.0, v88
	v_mul_f32_e32 v89, 0xbfb8aa3b, v89
	global_store_dwordx4 v[114:115], v[98:101], off offset:256
	v_exp_f32_e32 v89, v89
	v_pk_mul_f32 v[90:91], v[90:91], s[58:59] op_sel_hi:[1,0]
	v_rcp_f32_e32 v100, v88
	v_add_f32_e32 v88, 1.0, v93
	v_mul_f32_e32 v93, 0xbfb8aa3b, v94
	v_exp_f32_e32 v93, v93
	v_add_f32_e32 v89, 1.0, v89
	v_mul_f32_e32 v90, 0xbfb8aa3b, v90
	v_mul_f32_e32 v92, 0xbfb8aa3b, v92
	v_exp_f32_e32 v90, v90
	v_rcp_f32_e32 v94, v89
	v_add_f32_e32 v89, 1.0, v93
	v_mul_f32_e32 v93, 0xbfb8aa3b, v95
	v_mul_f32_e32 v91, 0xbfb8aa3b, v91
	v_exp_f32_e32 v92, v92
	v_exp_f32_e32 v93, v93
	v_exp_f32_e32 v91, v91
	v_add_f32_e32 v90, 1.0, v90
	v_pk_mul_f32 v[80:81], v[80:81], s[58:59] op_sel_hi:[1,0]
	v_add_f32_e32 v92, 1.0, v92
	v_rcp_f32_e32 v95, v90
	v_add_f32_e32 v90, 1.0, v93
	v_add_f32_e32 v91, 1.0, v91
	v_pk_mul_f32 v[84:85], v[84:85], s[58:59] op_sel_hi:[1,0]
	v_mul_f32_e32 v80, 0xbfb8aa3b, v80
	v_or_b32_e32 v98, 32, v96
	v_rcp_f32_e32 v92, v92
	v_rcp_f32_e32 v88, v88
	v_rcp_f32_e32 v89, v89
	v_rcp_f32_e32 v90, v90
	v_rcp_f32_e32 v91, v91
	v_exp_f32_e32 v80, v80
	v_mul_f32_e32 v85, 0xbfb8aa3b, v85
	v_mad_i64_i32 v[98:99], s[18:19], v98, s59, v[132:133]
	v_exp_f32_e32 v85, v85
	v_lshl_add_u64 v[98:99], v[98:99], 0, s[16:17]
	v_lshl_add_u64 v[98:99], v[98:99], 0, s[76:77]
	v_lshl_add_u64 v[98:99], v[98:99], 0, v[206:207]
	v_cvt_pk_bf16_f32 v88, v92, v88
	v_cvt_pk_bf16_f32 v89, v89, v90
	v_cvt_pk_bf16_f32 v90, v100, v94
	v_cvt_pk_bf16_f32 v91, v95, v91
	v_pk_mul_f32 v[86:87], v[86:87], s[58:59] op_sel_hi:[1,0]
	v_add_f32_e32 v80, 1.0, v80
	v_mul_f32_e32 v81, 0xbfb8aa3b, v81
	global_store_dwordx4 v[98:99], v[88:91], off
	v_exp_f32_e32 v81, v81
	v_pk_mul_f32 v[82:83], v[82:83], s[58:59] op_sel_hi:[1,0]
	v_rcp_f32_e32 v88, v80
	v_add_f32_e32 v80, 1.0, v85
	v_mul_f32_e32 v85, 0xbfb8aa3b, v86
	v_exp_f32_e32 v85, v85
	v_add_f32_e32 v81, 1.0, v81
	v_mul_f32_e32 v82, 0xbfb8aa3b, v82
	v_mul_f32_e32 v84, 0xbfb8aa3b, v84
	v_exp_f32_e32 v82, v82
	v_rcp_f32_e32 v86, v81
	v_add_f32_e32 v81, 1.0, v85
	v_mul_f32_e32 v85, 0xbfb8aa3b, v87
	v_mul_f32_e32 v83, 0xbfb8aa3b, v83
	v_exp_f32_e32 v84, v84
	v_exp_f32_e32 v85, v85
	v_exp_f32_e32 v83, v83
	v_add_f32_e32 v82, 1.0, v82
	v_pk_mul_f32 v[72:73], v[72:73], s[58:59] op_sel_hi:[1,0]
	v_add_f32_e32 v84, 1.0, v84
	v_rcp_f32_e32 v87, v82
	v_add_f32_e32 v82, 1.0, v85
	v_add_f32_e32 v83, 1.0, v83
	v_pk_mul_f32 v[76:77], v[76:77], s[58:59] op_sel_hi:[1,0]
	v_mul_f32_e32 v72, 0xbfb8aa3b, v72
	v_rcp_f32_e32 v84, v84
	v_rcp_f32_e32 v80, v80
	v_rcp_f32_e32 v81, v81
	v_rcp_f32_e32 v82, v82
	v_rcp_f32_e32 v83, v83
	v_exp_f32_e32 v72, v72
	v_mul_f32_e32 v77, 0xbfb8aa3b, v77
	v_exp_f32_e32 v77, v77
	v_cvt_pk_bf16_f32 v80, v84, v80
	v_cvt_pk_bf16_f32 v81, v81, v82
	v_cvt_pk_bf16_f32 v82, v88, v86
	v_cvt_pk_bf16_f32 v83, v87, v83
	v_pk_mul_f32 v[78:79], v[78:79], s[58:59] op_sel_hi:[1,0]
	v_add_f32_e32 v72, 1.0, v72
	v_mul_f32_e32 v73, 0xbfb8aa3b, v73
	global_store_dwordx4 v[98:99], v[80:83], off offset:256
	v_exp_f32_e32 v73, v73
	v_pk_mul_f32 v[74:75], v[74:75], s[58:59] op_sel_hi:[1,0]
	v_rcp_f32_e32 v82, v72
	v_add_f32_e32 v72, 1.0, v77
	v_mul_f32_e32 v77, 0xbfb8aa3b, v78
	v_exp_f32_e32 v77, v77
	v_add_f32_e32 v73, 1.0, v73
	v_mul_f32_e32 v74, 0xbfb8aa3b, v74
	v_mul_f32_e32 v76, 0xbfb8aa3b, v76
	v_exp_f32_e32 v74, v74
	v_rcp_f32_e32 v78, v73
	v_add_f32_e32 v73, 1.0, v77
	v_mul_f32_e32 v77, 0xbfb8aa3b, v79
	v_mul_f32_e32 v75, 0xbfb8aa3b, v75
	v_exp_f32_e32 v76, v76
	v_exp_f32_e32 v77, v77
	v_exp_f32_e32 v75, v75
	v_add_f32_e32 v74, 1.0, v74
	v_pk_mul_f32 v[64:65], v[64:65], s[58:59] op_sel_hi:[1,0]
	v_add_f32_e32 v76, 1.0, v76
	v_rcp_f32_e32 v79, v74
	v_add_f32_e32 v74, 1.0, v77
	v_add_f32_e32 v75, 1.0, v75
	v_pk_mul_f32 v[68:69], v[68:69], s[58:59] op_sel_hi:[1,0]
	v_mul_f32_e32 v64, 0xbfb8aa3b, v64
	v_or_b32_e32 v80, 48, v96
	v_rcp_f32_e32 v76, v76
	v_rcp_f32_e32 v72, v72
	v_rcp_f32_e32 v73, v73
	v_rcp_f32_e32 v74, v74
	v_rcp_f32_e32 v75, v75
	v_exp_f32_e32 v64, v64
	v_mul_f32_e32 v69, 0xbfb8aa3b, v69
	v_mad_i64_i32 v[80:81], s[18:19], v80, s59, v[132:133]
	v_exp_f32_e32 v69, v69
	v_lshl_add_u64 v[80:81], v[80:81], 0, s[16:17]
	v_lshl_add_u64 v[80:81], v[80:81], 0, s[76:77]
	v_lshl_add_u64 v[80:81], v[80:81], 0, v[206:207]
	v_cvt_pk_bf16_f32 v72, v76, v72
	v_cvt_pk_bf16_f32 v73, v73, v74
	v_cvt_pk_bf16_f32 v74, v82, v78
	v_cvt_pk_bf16_f32 v75, v79, v75
	v_pk_mul_f32 v[70:71], v[70:71], s[58:59] op_sel_hi:[1,0]
	v_add_f32_e32 v64, 1.0, v64
	v_mul_f32_e32 v65, 0xbfb8aa3b, v65
	global_store_dwordx4 v[80:81], v[72:75], off
	v_exp_f32_e32 v65, v65
	v_pk_mul_f32 v[66:67], v[66:67], s[58:59] op_sel_hi:[1,0]
	v_rcp_f32_e32 v72, v64
	v_add_f32_e32 v64, 1.0, v69
	v_mul_f32_e32 v69, 0xbfb8aa3b, v70
	v_exp_f32_e32 v69, v69
	v_add_f32_e32 v65, 1.0, v65
	v_mul_f32_e32 v66, 0xbfb8aa3b, v66
	v_mul_f32_e32 v68, 0xbfb8aa3b, v68
	v_exp_f32_e32 v66, v66
	v_rcp_f32_e32 v70, v65
	v_add_f32_e32 v65, 1.0, v69
	v_mul_f32_e32 v69, 0xbfb8aa3b, v71
	v_mul_f32_e32 v67, 0xbfb8aa3b, v67
	v_exp_f32_e32 v68, v68
	v_exp_f32_e32 v69, v69
	v_exp_f32_e32 v67, v67
	v_add_f32_e32 v66, 1.0, v66
	v_pk_mul_f32 v[56:57], v[56:57], s[58:59] op_sel_hi:[1,0]
	v_add_f32_e32 v68, 1.0, v68
	v_rcp_f32_e32 v71, v66
	v_add_f32_e32 v66, 1.0, v69
	v_add_f32_e32 v67, 1.0, v67
	v_pk_mul_f32 v[60:61], v[60:61], s[58:59] op_sel_hi:[1,0]
	v_mul_f32_e32 v56, 0xbfb8aa3b, v56
	v_rcp_f32_e32 v68, v68
	v_rcp_f32_e32 v64, v64
	v_rcp_f32_e32 v65, v65
	v_rcp_f32_e32 v66, v66
	v_rcp_f32_e32 v67, v67
	v_exp_f32_e32 v56, v56
	v_mul_f32_e32 v61, 0xbfb8aa3b, v61
	v_exp_f32_e32 v61, v61
	v_cvt_pk_bf16_f32 v64, v68, v64
	v_cvt_pk_bf16_f32 v65, v65, v66
	v_cvt_pk_bf16_f32 v66, v72, v70
	v_cvt_pk_bf16_f32 v67, v71, v67
	v_pk_mul_f32 v[62:63], v[62:63], s[58:59] op_sel_hi:[1,0]
	v_add_f32_e32 v56, 1.0, v56
	v_mul_f32_e32 v57, 0xbfb8aa3b, v57
	global_store_dwordx4 v[80:81], v[64:67], off offset:256
	v_exp_f32_e32 v57, v57
	v_pk_mul_f32 v[58:59], v[58:59], s[58:59] op_sel_hi:[1,0]
	v_rcp_f32_e32 v66, v56
	v_add_f32_e32 v56, 1.0, v61
	v_mul_f32_e32 v61, 0xbfb8aa3b, v62
	v_exp_f32_e32 v61, v61
	v_add_f32_e32 v57, 1.0, v57
	v_mul_f32_e32 v58, 0xbfb8aa3b, v58
	v_mul_f32_e32 v60, 0xbfb8aa3b, v60
	v_exp_f32_e32 v58, v58
	v_rcp_f32_e32 v62, v57
	v_add_f32_e32 v57, 1.0, v61
	v_mul_f32_e32 v61, 0xbfb8aa3b, v63
	v_mul_f32_e32 v59, 0xbfb8aa3b, v59
	v_exp_f32_e32 v60, v60
	v_exp_f32_e32 v61, v61
	v_exp_f32_e32 v59, v59
	v_add_f32_e32 v58, 1.0, v58
	v_pk_mul_f32 v[48:49], v[48:49], s[58:59] op_sel_hi:[1,0]
	v_add_f32_e32 v60, 1.0, v60
	v_rcp_f32_e32 v63, v58
	v_add_f32_e32 v58, 1.0, v61
	v_add_f32_e32 v59, 1.0, v59
	v_pk_mul_f32 v[52:53], v[52:53], s[58:59] op_sel_hi:[1,0]
	v_mul_f32_e32 v48, 0xbfb8aa3b, v48
	v_add_u32_e32 v64, 0x80, v96
	v_rcp_f32_e32 v60, v60
	v_rcp_f32_e32 v56, v56
	v_rcp_f32_e32 v57, v57
	v_rcp_f32_e32 v58, v58
	v_rcp_f32_e32 v59, v59
	v_exp_f32_e32 v48, v48
	v_mul_f32_e32 v53, 0xbfb8aa3b, v53
	v_mad_i64_i32 v[64:65], s[18:19], v64, s59, v[132:133]
	v_exp_f32_e32 v53, v53
	v_lshl_add_u64 v[64:65], v[64:65], 0, s[16:17]
	v_lshl_add_u64 v[64:65], v[64:65], 0, s[76:77]
	v_lshl_add_u64 v[64:65], v[64:65], 0, v[206:207]
	v_cvt_pk_bf16_f32 v56, v60, v56
	v_cvt_pk_bf16_f32 v57, v57, v58
	v_cvt_pk_bf16_f32 v58, v66, v62
	v_cvt_pk_bf16_f32 v59, v63, v59
	v_pk_mul_f32 v[54:55], v[54:55], s[58:59] op_sel_hi:[1,0]
	v_add_f32_e32 v48, 1.0, v48
	v_mul_f32_e32 v49, 0xbfb8aa3b, v49
	global_store_dwordx4 v[64:65], v[56:59], off
	v_exp_f32_e32 v49, v49
	v_pk_mul_f32 v[50:51], v[50:51], s[58:59] op_sel_hi:[1,0]
	v_rcp_f32_e32 v56, v48
	v_add_f32_e32 v48, 1.0, v53
	v_mul_f32_e32 v53, 0xbfb8aa3b, v54
	v_exp_f32_e32 v53, v53
	v_add_f32_e32 v49, 1.0, v49
	v_mul_f32_e32 v50, 0xbfb8aa3b, v50
	v_mul_f32_e32 v52, 0xbfb8aa3b, v52
	v_exp_f32_e32 v50, v50
	v_rcp_f32_e32 v54, v49
	v_add_f32_e32 v49, 1.0, v53
	v_mul_f32_e32 v53, 0xbfb8aa3b, v55
	v_mul_f32_e32 v51, 0xbfb8aa3b, v51
	v_exp_f32_e32 v52, v52
	v_exp_f32_e32 v53, v53
	v_exp_f32_e32 v51, v51
	v_add_f32_e32 v50, 1.0, v50
	v_pk_mul_f32 v[40:41], v[40:41], s[58:59] op_sel_hi:[1,0]
	v_add_f32_e32 v52, 1.0, v52
	v_rcp_f32_e32 v55, v50
	v_add_f32_e32 v50, 1.0, v53
	v_add_f32_e32 v51, 1.0, v51
	v_pk_mul_f32 v[44:45], v[44:45], s[58:59] op_sel_hi:[1,0]
	v_mul_f32_e32 v40, 0xbfb8aa3b, v40
	v_rcp_f32_e32 v52, v52
	v_rcp_f32_e32 v48, v48
	v_rcp_f32_e32 v49, v49
	v_rcp_f32_e32 v50, v50
	v_rcp_f32_e32 v51, v51
	v_exp_f32_e32 v40, v40
	v_mul_f32_e32 v45, 0xbfb8aa3b, v45
	v_exp_f32_e32 v45, v45
	v_cvt_pk_bf16_f32 v48, v52, v48
	v_cvt_pk_bf16_f32 v49, v49, v50
	v_cvt_pk_bf16_f32 v50, v56, v54
	v_cvt_pk_bf16_f32 v51, v55, v51
	v_pk_mul_f32 v[46:47], v[46:47], s[58:59] op_sel_hi:[1,0]
	v_add_f32_e32 v40, 1.0, v40
	v_mul_f32_e32 v41, 0xbfb8aa3b, v41
	global_store_dwordx4 v[64:65], v[48:51], off offset:256
	v_exp_f32_e32 v41, v41
	v_pk_mul_f32 v[42:43], v[42:43], s[58:59] op_sel_hi:[1,0]
	v_rcp_f32_e32 v50, v40
	v_add_f32_e32 v40, 1.0, v45
	v_mul_f32_e32 v45, 0xbfb8aa3b, v46
	v_exp_f32_e32 v45, v45
	v_add_f32_e32 v41, 1.0, v41
	v_mul_f32_e32 v42, 0xbfb8aa3b, v42
	v_mul_f32_e32 v44, 0xbfb8aa3b, v44
	v_exp_f32_e32 v42, v42
	v_rcp_f32_e32 v46, v41
	v_add_f32_e32 v41, 1.0, v45
	v_mul_f32_e32 v45, 0xbfb8aa3b, v47
	v_mul_f32_e32 v43, 0xbfb8aa3b, v43
	v_exp_f32_e32 v44, v44
	v_exp_f32_e32 v45, v45
	v_exp_f32_e32 v43, v43
	v_add_f32_e32 v42, 1.0, v42
	v_pk_mul_f32 v[32:33], v[32:33], s[58:59] op_sel_hi:[1,0]
	v_add_f32_e32 v44, 1.0, v44
	v_rcp_f32_e32 v47, v42
	v_add_f32_e32 v42, 1.0, v45
	v_add_f32_e32 v43, 1.0, v43
	v_pk_mul_f32 v[36:37], v[36:37], s[58:59] op_sel_hi:[1,0]
	v_mul_f32_e32 v32, 0xbfb8aa3b, v32
	v_add_u32_e32 v48, 0x90, v96
	v_rcp_f32_e32 v44, v44
	v_rcp_f32_e32 v40, v40
	v_rcp_f32_e32 v41, v41
	v_rcp_f32_e32 v42, v42
	v_rcp_f32_e32 v43, v43
	v_exp_f32_e32 v32, v32
	v_mul_f32_e32 v37, 0xbfb8aa3b, v37
	v_mad_i64_i32 v[48:49], s[18:19], v48, s59, v[132:133]
	v_exp_f32_e32 v37, v37
	v_lshl_add_u64 v[48:49], v[48:49], 0, s[16:17]
	v_lshl_add_u64 v[48:49], v[48:49], 0, s[76:77]
	v_lshl_add_u64 v[48:49], v[48:49], 0, v[206:207]
	v_cvt_pk_bf16_f32 v40, v44, v40
	v_cvt_pk_bf16_f32 v41, v41, v42
	v_cvt_pk_bf16_f32 v42, v50, v46
	v_cvt_pk_bf16_f32 v43, v47, v43
	v_pk_mul_f32 v[38:39], v[38:39], s[58:59] op_sel_hi:[1,0]
	v_add_f32_e32 v32, 1.0, v32
	v_mul_f32_e32 v33, 0xbfb8aa3b, v33
	global_store_dwordx4 v[48:49], v[40:43], off
	v_exp_f32_e32 v33, v33
	v_pk_mul_f32 v[34:35], v[34:35], s[58:59] op_sel_hi:[1,0]
	v_rcp_f32_e32 v40, v32
	v_add_f32_e32 v32, 1.0, v37
	v_mul_f32_e32 v37, 0xbfb8aa3b, v38
	v_exp_f32_e32 v37, v37
	v_add_f32_e32 v33, 1.0, v33
	v_mul_f32_e32 v34, 0xbfb8aa3b, v34
	v_mul_f32_e32 v36, 0xbfb8aa3b, v36
	v_exp_f32_e32 v34, v34
	v_rcp_f32_e32 v38, v33
	v_add_f32_e32 v33, 1.0, v37
	v_mul_f32_e32 v37, 0xbfb8aa3b, v39
	v_mul_f32_e32 v35, 0xbfb8aa3b, v35
	v_exp_f32_e32 v36, v36
	v_exp_f32_e32 v37, v37
	v_exp_f32_e32 v35, v35
	v_add_f32_e32 v34, 1.0, v34
	v_pk_mul_f32 v[24:25], v[24:25], s[58:59] op_sel_hi:[1,0]
	v_add_f32_e32 v36, 1.0, v36
	v_rcp_f32_e32 v39, v34
	v_add_f32_e32 v34, 1.0, v37
	v_add_f32_e32 v35, 1.0, v35
	v_pk_mul_f32 v[28:29], v[28:29], s[58:59] op_sel_hi:[1,0]
	v_mul_f32_e32 v24, 0xbfb8aa3b, v24
	v_rcp_f32_e32 v36, v36
	v_rcp_f32_e32 v32, v32
	v_rcp_f32_e32 v33, v33
	v_rcp_f32_e32 v34, v34
	v_rcp_f32_e32 v35, v35
	v_exp_f32_e32 v24, v24
	v_mul_f32_e32 v29, 0xbfb8aa3b, v29
	v_exp_f32_e32 v29, v29
	v_cvt_pk_bf16_f32 v32, v36, v32
	v_cvt_pk_bf16_f32 v33, v33, v34
	v_cvt_pk_bf16_f32 v34, v40, v38
	v_cvt_pk_bf16_f32 v35, v39, v35
	v_pk_mul_f32 v[30:31], v[30:31], s[58:59] op_sel_hi:[1,0]
	v_add_f32_e32 v24, 1.0, v24
	v_mul_f32_e32 v25, 0xbfb8aa3b, v25
	global_store_dwordx4 v[48:49], v[32:35], off offset:256
	v_exp_f32_e32 v25, v25
	v_pk_mul_f32 v[26:27], v[26:27], s[58:59] op_sel_hi:[1,0]
	v_rcp_f32_e32 v34, v24
	v_add_f32_e32 v24, 1.0, v29
	v_mul_f32_e32 v29, 0xbfb8aa3b, v30
	v_exp_f32_e32 v29, v29
	v_add_f32_e32 v25, 1.0, v25
	v_mul_f32_e32 v26, 0xbfb8aa3b, v26
	v_mul_f32_e32 v28, 0xbfb8aa3b, v28
	v_exp_f32_e32 v26, v26
	v_rcp_f32_e32 v30, v25
	v_add_f32_e32 v25, 1.0, v29
	v_mul_f32_e32 v29, 0xbfb8aa3b, v31
	v_mul_f32_e32 v27, 0xbfb8aa3b, v27
	v_exp_f32_e32 v28, v28
	v_exp_f32_e32 v29, v29
	v_exp_f32_e32 v27, v27
	v_add_f32_e32 v26, 1.0, v26
	v_pk_mul_f32 v[16:17], v[16:17], s[58:59] op_sel_hi:[1,0]
	v_add_f32_e32 v28, 1.0, v28
	v_rcp_f32_e32 v31, v26
	v_add_f32_e32 v26, 1.0, v29
	v_add_f32_e32 v27, 1.0, v27
	v_pk_mul_f32 v[20:21], v[20:21], s[58:59] op_sel_hi:[1,0]
	v_mul_f32_e32 v16, 0xbfb8aa3b, v16
	v_add_u32_e32 v32, 0xa0, v96
	v_rcp_f32_e32 v28, v28
	v_rcp_f32_e32 v24, v24
	v_rcp_f32_e32 v25, v25
	v_rcp_f32_e32 v26, v26
	v_rcp_f32_e32 v27, v27
	v_exp_f32_e32 v16, v16
	v_mul_f32_e32 v21, 0xbfb8aa3b, v21
	v_mad_i64_i32 v[32:33], s[18:19], v32, s59, v[132:133]
	v_exp_f32_e32 v21, v21
	v_lshl_add_u64 v[32:33], v[32:33], 0, s[16:17]
	v_lshl_add_u64 v[32:33], v[32:33], 0, s[76:77]
	v_lshl_add_u64 v[32:33], v[32:33], 0, v[206:207]
	v_cvt_pk_bf16_f32 v24, v28, v24
	v_cvt_pk_bf16_f32 v25, v25, v26
	v_cvt_pk_bf16_f32 v26, v34, v30
	v_cvt_pk_bf16_f32 v27, v31, v27
	v_pk_mul_f32 v[22:23], v[22:23], s[58:59] op_sel_hi:[1,0]
	v_add_f32_e32 v16, 1.0, v16
	v_mul_f32_e32 v17, 0xbfb8aa3b, v17
	global_store_dwordx4 v[32:33], v[24:27], off
	v_exp_f32_e32 v17, v17
	v_pk_mul_f32 v[18:19], v[18:19], s[58:59] op_sel_hi:[1,0]
	v_rcp_f32_e32 v24, v16
	v_add_f32_e32 v16, 1.0, v21
	v_mul_f32_e32 v21, 0xbfb8aa3b, v22
	v_exp_f32_e32 v21, v21
	v_add_f32_e32 v17, 1.0, v17
	v_mul_f32_e32 v18, 0xbfb8aa3b, v18
	v_mul_f32_e32 v20, 0xbfb8aa3b, v20
	v_exp_f32_e32 v18, v18
	v_rcp_f32_e32 v22, v17
	v_add_f32_e32 v17, 1.0, v21
	v_mul_f32_e32 v21, 0xbfb8aa3b, v23
	v_mul_f32_e32 v19, 0xbfb8aa3b, v19
	v_exp_f32_e32 v20, v20
	v_exp_f32_e32 v21, v21
	v_exp_f32_e32 v19, v19
	v_add_f32_e32 v18, 1.0, v18
	v_pk_mul_f32 v[8:9], v[8:9], s[58:59] op_sel_hi:[1,0]
	v_add_f32_e32 v20, 1.0, v20
	v_rcp_f32_e32 v23, v18
	v_add_f32_e32 v18, 1.0, v21
	v_add_f32_e32 v19, 1.0, v19
	v_pk_mul_f32 v[12:13], v[12:13], s[58:59] op_sel_hi:[1,0]
	v_mul_f32_e32 v8, 0xbfb8aa3b, v8
	v_rcp_f32_e32 v20, v20
	v_rcp_f32_e32 v16, v16
	v_rcp_f32_e32 v17, v17
	v_rcp_f32_e32 v18, v18
	v_rcp_f32_e32 v19, v19
	v_exp_f32_e32 v8, v8
	v_mul_f32_e32 v13, 0xbfb8aa3b, v13
	v_exp_f32_e32 v13, v13
	v_cvt_pk_bf16_f32 v16, v20, v16
	v_cvt_pk_bf16_f32 v17, v17, v18
	v_cvt_pk_bf16_f32 v18, v24, v22
	v_cvt_pk_bf16_f32 v19, v23, v19
	v_pk_mul_f32 v[14:15], v[14:15], s[58:59] op_sel_hi:[1,0]
	v_add_f32_e32 v8, 1.0, v8
	v_mul_f32_e32 v9, 0xbfb8aa3b, v9
	global_store_dwordx4 v[32:33], v[16:19], off offset:256
	v_exp_f32_e32 v9, v9
	v_pk_mul_f32 v[10:11], v[10:11], s[58:59] op_sel_hi:[1,0]
	v_rcp_f32_e32 v18, v8
	v_add_f32_e32 v8, 1.0, v13
	v_mul_f32_e32 v13, 0xbfb8aa3b, v14
	v_exp_f32_e32 v13, v13
	v_add_f32_e32 v9, 1.0, v9
	v_mul_f32_e32 v10, 0xbfb8aa3b, v10
	v_mul_f32_e32 v12, 0xbfb8aa3b, v12
	v_exp_f32_e32 v10, v10
	v_rcp_f32_e32 v14, v9
	v_add_f32_e32 v9, 1.0, v13
	v_mul_f32_e32 v13, 0xbfb8aa3b, v15
	v_mul_f32_e32 v11, 0xbfb8aa3b, v11
	v_exp_f32_e32 v12, v12
	v_exp_f32_e32 v13, v13
	v_exp_f32_e32 v11, v11
	v_add_f32_e32 v10, 1.0, v10
	v_pk_mul_f32 v[0:1], v[0:1], s[58:59] op_sel_hi:[1,0]
	v_add_f32_e32 v12, 1.0, v12
	v_rcp_f32_e32 v15, v10
	v_add_f32_e32 v10, 1.0, v13
	v_add_f32_e32 v11, 1.0, v11
	v_pk_mul_f32 v[4:5], v[4:5], s[58:59] op_sel_hi:[1,0]
	v_mul_f32_e32 v0, 0xbfb8aa3b, v0
	v_add_u32_e32 v16, 0xb0, v96
	v_rcp_f32_e32 v12, v12
	v_rcp_f32_e32 v8, v8
	v_rcp_f32_e32 v9, v9
	v_rcp_f32_e32 v10, v10
	v_rcp_f32_e32 v11, v11
	v_exp_f32_e32 v0, v0
	v_mul_f32_e32 v5, 0xbfb8aa3b, v5
	v_mad_i64_i32 v[16:17], s[18:19], v16, s59, v[132:133]
	v_exp_f32_e32 v5, v5
	v_lshl_add_u64 v[16:17], v[16:17], 0, s[16:17]
	v_lshl_add_u64 v[16:17], v[16:17], 0, s[76:77]
	v_lshl_add_u64 v[16:17], v[16:17], 0, v[206:207]
	v_cvt_pk_bf16_f32 v8, v12, v8
	v_cvt_pk_bf16_f32 v9, v9, v10
	v_cvt_pk_bf16_f32 v10, v18, v14
	v_cvt_pk_bf16_f32 v11, v15, v11
	v_pk_mul_f32 v[6:7], v[6:7], s[58:59] op_sel_hi:[1,0]
	v_add_f32_e32 v0, 1.0, v0
	v_mul_f32_e32 v1, 0xbfb8aa3b, v1
	global_store_dwordx4 v[16:17], v[8:11], off
	v_exp_f32_e32 v1, v1
	v_pk_mul_f32 v[2:3], v[2:3], s[58:59] op_sel_hi:[1,0]
	v_rcp_f32_e32 v8, v0
	v_add_f32_e32 v0, 1.0, v5
	v_mul_f32_e32 v5, 0xbfb8aa3b, v6
	v_exp_f32_e32 v5, v5
	v_add_f32_e32 v1, 1.0, v1
	v_mul_f32_e32 v2, 0xbfb8aa3b, v2
	v_mul_f32_e32 v4, 0xbfb8aa3b, v4
	v_exp_f32_e32 v2, v2
	v_rcp_f32_e32 v6, v1
	v_add_f32_e32 v1, 1.0, v5
	v_mul_f32_e32 v5, 0xbfb8aa3b, v7
	v_mul_f32_e32 v3, 0xbfb8aa3b, v3
	v_exp_f32_e32 v4, v4
	v_exp_f32_e32 v5, v5
	v_exp_f32_e32 v3, v3
	v_add_f32_e32 v2, 1.0, v2
	v_add_f32_e32 v4, 1.0, v4
	v_rcp_f32_e32 v7, v2
	v_add_f32_e32 v2, 1.0, v5
	v_add_f32_e32 v3, 1.0, v3
	v_rcp_f32_e32 v4, v4
	v_rcp_f32_e32 v0, v0
	v_rcp_f32_e32 v1, v1
	v_rcp_f32_e32 v2, v2
	v_rcp_f32_e32 v3, v3
	v_cvt_pk_bf16_f32 v0, v4, v0
	s_cmp_eq_u32 s40, s36
	v_cvt_pk_bf16_f32 v1, v1, v2
	v_cvt_pk_bf16_f32 v2, v8, v6
	v_cvt_pk_bf16_f32 v3, v7, v3
	s_mov_b64 s[16:17], -1
	global_store_dwordx4 v[16:17], v[0:3], off offset:256
	s_cbranch_scc1 .LBB0_366
	s_andn2_b64 vcc, exec, s[2:3]
	s_branch .LBB0_365

.Lmy_peel1370_exit:
	s_cmp_lg_u32 s39, s42
	s_cbranch_scc1 .LBB0_1373
	s_and_b64 vcc, exec, s[14:15]
	s_cbranch_vccz .LBB0_1373
	s_barrier
.LBB0_1373:
	s_lshl_b32 s22, s78, 8
	s_min_i32 s20, s22, 0x2000
	s_ashr_i32 s20, s20, 11
	v_lshl_or_b32 v130, s76, 8, v156
	s_mul_hi_i32 s21, s20, 0xc000
	s_mul_i32 s20, s20, 0xc000
	s_add_u32 s20, s55, s20
	v_ashrrev_i32_e32 v131, 31, v130
	v_add_u32_e32 v148, s22, v154
	s_addc_u32 s21, s69, s21
	v_lshlrev_b64 v[146:147], 2, v[130:131]
	v_ashrrev_i32_e32 v149, 31, v148
	v_lshl_add_u64 v[130:131], s[20:21], 0, v[146:147]
	v_lshlrev_b64 v[150:151], 13, v[148:149]
	v_add_co_u32_e32 v132, vcc, s62, v130
	v_lshl_add_u64 v[134:135], s[8:9], 0, v[150:151]
	v_add_u32_e32 v96, 0xffffe000, v148
	v_addc_co_u32_e32 v133, vcc, 0, v131, vcc
	v_lshl_add_u64 v[162:163], v[134:135], 0, v[146:147]
	v_lshlrev_b64 v[134:135], 13, v[96:97]
	v_lshl_add_u64 v[136:137], s[10:11], 0, v[150:151]
	v_lshl_add_u64 v[134:135], s[12:13], 0, v[134:135]
	v_cmp_gt_i32_e32 vcc, s53, v148
	s_mov_b64 s[20:21], 0x4000
	v_lshl_add_u64 v[130:131], v[130:131], 0, s[20:21]
	v_cndmask_b32_e32 v135, v135, v137, vcc
	v_cndmask_b32_e32 v134, v134, v136, vcc
	v_lshl_add_u64 v[134:135], v[134:135], 0, v[146:147]
	v_cndmask_b32_e64 v165, v135, v163, s[2:3]
	v_cndmask_b32_e64 v164, v134, v162, s[2:3]
	global_load_dwordx4 v[158:161], v[164:165], off
	global_load_dwordx4 v[142:145], v[132:133], off
	global_load_dwordx4 v[138:141], v[130:131], off offset:64
	global_load_dwordx4 v[134:137], v[130:131], off offset:512
	s_nop 0
	global_load_dwordx4 v[130:133], v[130:131], off offset:576
	v_add_u32_e32 v96, 0xffffe010, v148
	s_mov_b64 s[20:21], 0x100000
	s_cmp_eq_u32 s39, s42
	s_waitcnt vmcnt(0)
	v_pk_fma_f32 v[128:129], v[128:129], v[144:145], v[160:161]
	v_pk_fma_f32 v[126:127], v[126:127], v[142:143], v[158:159]
	global_store_dwordx4 v[162:163], v[126:129], off
	global_load_dwordx4 v[126:129], v[164:165], off offset:64
	s_waitcnt vmcnt(0)
	v_pk_fma_f32 v[124:125], v[124:125], v[140:141], v[128:129]
	v_pk_fma_f32 v[122:123], v[122:123], v[138:139], v[126:127]
	global_store_dwordx4 v[162:163], v[122:125], off offset:64
	global_load_dwordx4 v[122:125], v[164:165], off offset:512
	v_lshlrev_b64 v[126:127], 13, v[96:97]
	v_lshl_add_u64 v[126:127], s[12:13], 0, v[126:127]
	v_add_u32_e32 v96, 0xffffe020, v148
	s_waitcnt vmcnt(0)
	v_pk_fma_f32 v[120:121], v[120:121], v[136:137], v[124:125]
	v_pk_fma_f32 v[118:119], v[118:119], v[134:135], v[122:123]
	global_store_dwordx4 v[162:163], v[118:121], off offset:512
	global_load_dwordx4 v[118:121], v[164:165], off offset:576
	v_or_b32_e32 v122, 16, v148
	v_ashrrev_i32_e32 v123, 31, v122
	v_lshlrev_b64 v[124:125], 13, v[122:123]
	v_lshl_add_u64 v[128:129], s[8:9], 0, v[124:125]
	v_lshl_add_u64 v[124:125], s[10:11], 0, v[124:125]
	v_cmp_gt_i32_e32 vcc, s53, v122
	v_lshl_add_u64 v[128:129], v[128:129], 0, v[146:147]
	s_waitcnt vmcnt(0)
	v_pk_fma_f32 v[108:109], v[108:109], v[132:133], v[120:121]
	v_cndmask_b32_e32 v123, v127, v125, vcc
	v_cndmask_b32_e32 v122, v126, v124, vcc
	v_lshl_add_u64 v[122:123], v[122:123], 0, v[146:147]
	v_pk_fma_f32 v[106:107], v[106:107], v[130:131], v[118:119]
	v_cndmask_b32_e64 v123, v123, v129, s[2:3]
	v_cndmask_b32_e64 v122, v122, v128, s[2:3]
	global_store_dwordx4 v[162:163], v[106:109], off offset:576
	global_load_dwordx4 v[106:109], v[122:123], off
	s_waitcnt vmcnt(0)
	v_pk_fma_f32 v[108:109], v[116:117], v[144:145], v[108:109]
	v_pk_fma_f32 v[106:107], v[114:115], v[142:143], v[106:107]
	global_store_dwordx4 v[128:129], v[106:109], off
	global_load_dwordx4 v[106:109], v[122:123], off offset:64
	s_waitcnt vmcnt(0)
	v_pk_fma_f32 v[108:109], v[112:113], v[140:141], v[108:109]
	v_pk_fma_f32 v[106:107], v[110:111], v[138:139], v[106:107]
	global_store_dwordx4 v[128:129], v[106:109], off offset:64
	global_load_dwordx4 v[106:109], v[122:123], off offset:512
	v_lshlrev_b64 v[112:113], 13, v[96:97]
	v_lshl_add_u64 v[112:113], s[12:13], 0, v[112:113]
	v_add_u32_e32 v96, 0xffffe030, v148
	s_waitcnt vmcnt(0)
	v_pk_fma_f32 v[104:105], v[104:105], v[136:137], v[108:109]
	v_pk_fma_f32 v[102:103], v[102:103], v[134:135], v[106:107]
	global_store_dwordx4 v[128:129], v[102:105], off offset:512
	global_load_dwordx4 v[102:105], v[122:123], off offset:576
	v_or_b32_e32 v106, 32, v148
	v_ashrrev_i32_e32 v107, 31, v106
	v_lshlrev_b64 v[108:109], 13, v[106:107]
	v_lshl_add_u64 v[110:111], s[8:9], 0, v[108:109]
	v_lshl_add_u64 v[108:109], s[10:11], 0, v[108:109]
	v_cmp_gt_i32_e32 vcc, s53, v106
	v_lshl_add_u64 v[110:111], v[110:111], 0, v[146:147]
	s_waitcnt vmcnt(0)
	v_pk_fma_f32 v[90:91], v[90:91], v[132:133], v[104:105]
	v_cndmask_b32_e32 v107, v113, v109, vcc
	v_cndmask_b32_e32 v106, v112, v108, vcc
	v_lshl_add_u64 v[106:107], v[106:107], 0, v[146:147]
	v_pk_fma_f32 v[88:89], v[88:89], v[130:131], v[102:103]
	v_cndmask_b32_e64 v107, v107, v111, s[2:3]
	v_cndmask_b32_e64 v106, v106, v110, s[2:3]
	global_store_dwordx4 v[128:129], v[88:91], off offset:576
	global_load_dwordx4 v[88:91], v[106:107], off
	s_waitcnt vmcnt(0)
	v_pk_fma_f32 v[90:91], v[100:101], v[144:145], v[90:91]
	v_pk_fma_f32 v[88:89], v[98:99], v[142:143], v[88:89]
	global_store_dwordx4 v[110:111], v[88:91], off
	global_load_dwordx4 v[88:91], v[106:107], off offset:64
	s_waitcnt vmcnt(0)
	v_pk_fma_f32 v[90:91], v[94:95], v[140:141], v[90:91]
	v_pk_fma_f32 v[88:89], v[92:93], v[138:139], v[88:89]
	global_store_dwordx4 v[110:111], v[88:91], off offset:64
	global_load_dwordx4 v[88:91], v[106:107], off offset:512
	v_lshlrev_b64 v[94:95], 13, v[96:97]
	v_lshl_add_u64 v[94:95], s[12:13], 0, v[94:95]
	v_add_u32_e32 v96, 0xffffe080, v148
	s_waitcnt vmcnt(0)
	v_pk_fma_f32 v[86:87], v[86:87], v[136:137], v[90:91]
	v_pk_fma_f32 v[84:85], v[84:85], v[134:135], v[88:89]
	global_store_dwordx4 v[110:111], v[84:87], off offset:512
	global_load_dwordx4 v[84:87], v[106:107], off offset:576
	v_or_b32_e32 v88, 48, v148
	v_ashrrev_i32_e32 v89, 31, v88
	v_lshlrev_b64 v[90:91], 13, v[88:89]
	v_lshl_add_u64 v[92:93], s[8:9], 0, v[90:91]
	v_lshl_add_u64 v[90:91], s[10:11], 0, v[90:91]
	v_cmp_gt_i32_e32 vcc, s53, v88
	v_lshl_add_u64 v[92:93], v[92:93], 0, v[146:147]
	s_waitcnt vmcnt(0)
	v_pk_fma_f32 v[74:75], v[74:75], v[132:133], v[86:87]
	v_cndmask_b32_e32 v89, v95, v91, vcc
	v_cndmask_b32_e32 v88, v94, v90, vcc
	v_lshl_add_u64 v[88:89], v[88:89], 0, v[146:147]
	v_pk_fma_f32 v[72:73], v[72:73], v[130:131], v[84:85]
	v_cndmask_b32_e64 v89, v89, v93, s[2:3]
	v_cndmask_b32_e64 v88, v88, v92, s[2:3]
	global_store_dwordx4 v[110:111], v[72:75], off offset:576
	global_load_dwordx4 v[72:75], v[88:89], off
	s_waitcnt vmcnt(0)
	v_pk_fma_f32 v[74:75], v[82:83], v[144:145], v[74:75]
	v_pk_fma_f32 v[72:73], v[80:81], v[142:143], v[72:73]
	global_store_dwordx4 v[92:93], v[72:75], off
	global_load_dwordx4 v[72:75], v[88:89], off offset:64
	s_waitcnt vmcnt(0)
	v_pk_fma_f32 v[74:75], v[78:79], v[140:141], v[74:75]
	v_pk_fma_f32 v[72:73], v[76:77], v[138:139], v[72:73]
	global_store_dwordx4 v[92:93], v[72:75], off offset:64
	global_load_dwordx4 v[72:75], v[88:89], off offset:512
	v_lshlrev_b64 v[76:77], 13, v[96:97]
	v_lshl_add_u64 v[76:77], s[12:13], 0, v[76:77]
	v_add_u32_e32 v96, 0xffffe090, v148
	s_waitcnt vmcnt(0)
	v_pk_fma_f32 v[70:71], v[70:71], v[136:137], v[74:75]
	v_pk_fma_f32 v[68:69], v[68:69], v[134:135], v[72:73]
	global_store_dwordx4 v[92:93], v[68:71], off offset:512
	global_load_dwordx4 v[68:71], v[88:89], off offset:576
	v_lshl_add_u64 v[72:73], v[150:151], 0, s[20:21]
	s_movk_i32 s20, 0x1f80
	v_lshl_add_u64 v[74:75], s[8:9], 0, v[72:73]
	v_lshl_add_u64 v[72:73], s[10:11], 0, v[72:73]
	v_cmp_gt_i32_e32 vcc, s20, v148
	v_lshl_add_u64 v[74:75], v[74:75], 0, v[146:147]
	s_mov_b64 s[20:21], 0x120000
	v_cndmask_b32_e32 v73, v77, v73, vcc
	v_cndmask_b32_e32 v72, v76, v72, vcc
	v_lshl_add_u64 v[72:73], v[72:73], 0, v[146:147]
	v_cndmask_b32_e64 v73, v73, v75, s[2:3]
	v_cndmask_b32_e64 v72, v72, v74, s[2:3]
	s_waitcnt vmcnt(0)
	v_pk_fma_f32 v[62:63], v[62:63], v[132:133], v[70:71]
	v_pk_fma_f32 v[60:61], v[60:61], v[130:131], v[68:69]
	global_store_dwordx4 v[92:93], v[60:63], off offset:576
	global_load_dwordx4 v[60:63], v[72:73], off
	s_waitcnt vmcnt(0)
	v_pk_fma_f32 v[62:63], v[66:67], v[144:145], v[62:63]
	v_pk_fma_f32 v[60:61], v[64:65], v[142:143], v[60:61]
	global_store_dwordx4 v[74:75], v[60:63], off
	global_load_dwordx4 v[60:63], v[72:73], off offset:64
	s_waitcnt vmcnt(0)
	v_pk_fma_f32 v[58:59], v[58:59], v[140:141], v[62:63]
	v_pk_fma_f32 v[56:57], v[56:57], v[138:139], v[60:61]
	global_store_dwordx4 v[74:75], v[56:59], off offset:64
	global_load_dwordx4 v[56:59], v[72:73], off offset:512
	v_lshlrev_b64 v[60:61], 13, v[96:97]
	v_lshl_add_u64 v[60:61], s[12:13], 0, v[60:61]
	v_add_u32_e32 v96, 0xffffe0a0, v148
	s_waitcnt vmcnt(0)
	v_pk_fma_f32 v[54:55], v[54:55], v[136:137], v[58:59]
	v_pk_fma_f32 v[52:53], v[52:53], v[134:135], v[56:57]
	global_store_dwordx4 v[74:75], v[52:55], off offset:512
	global_load_dwordx4 v[52:55], v[72:73], off offset:576
	v_lshl_add_u64 v[56:57], v[150:151], 0, s[20:21]
	s_movk_i32 s20, 0x1f70
	v_lshl_add_u64 v[58:59], s[8:9], 0, v[56:57]
	v_lshl_add_u64 v[56:57], s[10:11], 0, v[56:57]
	v_cmp_gt_i32_e32 vcc, s20, v148
	v_lshl_add_u64 v[58:59], v[58:59], 0, v[146:147]
	s_mov_b64 s[20:21], 0x140000
	v_cndmask_b32_e32 v57, v61, v57, vcc
	v_cndmask_b32_e32 v56, v60, v56, vcc
	v_lshl_add_u64 v[56:57], v[56:57], 0, v[146:147]
	v_cndmask_b32_e64 v57, v57, v59, s[2:3]
	v_cndmask_b32_e64 v56, v56, v58, s[2:3]
	s_waitcnt vmcnt(0)
	v_pk_fma_f32 v[42:43], v[42:43], v[132:133], v[54:55]
	v_pk_fma_f32 v[40:41], v[40:41], v[130:131], v[52:53]
	global_store_dwordx4 v[74:75], v[40:43], off offset:576
	global_load_dwordx4 v[40:43], v[56:57], off
	s_waitcnt vmcnt(0)
	v_pk_fma_f32 v[42:43], v[50:51], v[144:145], v[42:43]
	v_pk_fma_f32 v[40:41], v[48:49], v[142:143], v[40:41]
	global_store_dwordx4 v[58:59], v[40:43], off
	global_load_dwordx4 v[40:43], v[56:57], off offset:64
	s_waitcnt vmcnt(0)
	v_pk_fma_f32 v[42:43], v[46:47], v[140:141], v[42:43]
	v_pk_fma_f32 v[40:41], v[44:45], v[138:139], v[40:41]
	global_store_dwordx4 v[58:59], v[40:43], off offset:64
	global_load_dwordx4 v[40:43], v[56:57], off offset:512
	v_lshlrev_b64 v[44:45], 13, v[96:97]
	v_lshl_add_u64 v[44:45], s[12:13], 0, v[44:45]
	v_add_u32_e32 v96, 0xffffe0b0, v148
	s_waitcnt vmcnt(0)
	v_pk_fma_f32 v[38:39], v[38:39], v[136:137], v[42:43]
	v_pk_fma_f32 v[36:37], v[36:37], v[134:135], v[40:41]
	global_store_dwordx4 v[58:59], v[36:39], off offset:512
	global_load_dwordx4 v[36:39], v[56:57], off offset:576
	v_lshl_add_u64 v[40:41], v[150:151], 0, s[20:21]
	s_movk_i32 s20, 0x1f60
	v_lshl_add_u64 v[42:43], s[8:9], 0, v[40:41]
	v_lshl_add_u64 v[40:41], s[10:11], 0, v[40:41]
	v_cmp_gt_i32_e32 vcc, s20, v148
	v_lshl_add_u64 v[42:43], v[42:43], 0, v[146:147]
	s_mov_b64 s[20:21], 0x160000
	v_cndmask_b32_e32 v41, v45, v41, vcc
	v_cndmask_b32_e32 v40, v44, v40, vcc
	v_lshl_add_u64 v[40:41], v[40:41], 0, v[146:147]
	v_cndmask_b32_e64 v41, v41, v43, s[2:3]
	v_cndmask_b32_e64 v40, v40, v42, s[2:3]
	s_waitcnt vmcnt(0)
	v_pk_fma_f32 v[26:27], v[26:27], v[132:133], v[38:39]
	v_pk_fma_f32 v[24:25], v[24:25], v[130:131], v[36:37]
	global_store_dwordx4 v[58:59], v[24:27], off offset:576
	global_load_dwordx4 v[24:27], v[40:41], off
	s_waitcnt vmcnt(0)
	v_pk_fma_f32 v[26:27], v[34:35], v[144:145], v[26:27]
	v_pk_fma_f32 v[24:25], v[32:33], v[142:143], v[24:25]
	global_store_dwordx4 v[42:43], v[24:27], off
	global_load_dwordx4 v[24:27], v[40:41], off offset:64
	s_waitcnt vmcnt(0)
	v_pk_fma_f32 v[26:27], v[30:31], v[140:141], v[26:27]
	v_pk_fma_f32 v[24:25], v[28:29], v[138:139], v[24:25]
	global_store_dwordx4 v[42:43], v[24:27], off offset:64
	global_load_dwordx4 v[24:27], v[40:41], off offset:512
	v_lshlrev_b64 v[28:29], 13, v[96:97]
	v_lshl_add_u64 v[28:29], s[12:13], 0, v[28:29]
	s_waitcnt vmcnt(0)
	v_pk_fma_f32 v[22:23], v[22:23], v[136:137], v[26:27]
	v_pk_fma_f32 v[20:21], v[20:21], v[134:135], v[24:25]
	global_store_dwordx4 v[42:43], v[20:23], off offset:512
	global_load_dwordx4 v[20:23], v[40:41], off offset:576
	v_lshl_add_u64 v[24:25], v[150:151], 0, s[20:21]
	s_movk_i32 s20, 0x1f50
	v_lshl_add_u64 v[26:27], s[8:9], 0, v[24:25]
	v_lshl_add_u64 v[24:25], s[10:11], 0, v[24:25]
	v_cmp_gt_i32_e32 vcc, s20, v148
	v_lshl_add_u64 v[26:27], v[26:27], 0, v[146:147]
	s_mov_b64 s[20:21], -1
	v_cndmask_b32_e32 v25, v29, v25, vcc
	v_cndmask_b32_e32 v24, v28, v24, vcc
	v_lshl_add_u64 v[24:25], v[24:25], 0, v[146:147]
	v_cndmask_b32_e64 v25, v25, v27, s[2:3]
	v_cndmask_b32_e64 v24, v24, v26, s[2:3]
	s_waitcnt vmcnt(0)
	v_pk_fma_f32 v[10:11], v[10:11], v[132:133], v[22:23]
	v_pk_fma_f32 v[8:9], v[8:9], v[130:131], v[20:21]
	global_store_dwordx4 v[42:43], v[8:11], off offset:576
	global_load_dwordx4 v[8:11], v[24:25], off
	s_waitcnt vmcnt(0)
	v_pk_fma_f32 v[10:11], v[18:19], v[144:145], v[10:11]
	v_pk_fma_f32 v[8:9], v[16:17], v[142:143], v[8:9]
	global_store_dwordx4 v[26:27], v[8:11], off
	global_load_dwordx4 v[8:11], v[24:25], off offset:64
	s_waitcnt vmcnt(0)
	v_pk_fma_f32 v[10:11], v[14:15], v[140:141], v[10:11]
	v_pk_fma_f32 v[8:9], v[12:13], v[138:139], v[8:9]
	global_store_dwordx4 v[26:27], v[8:11], off offset:64
	global_load_dwordx4 v[8:11], v[24:25], off offset:512
	s_waitcnt vmcnt(0)
	v_pk_fma_f32 v[6:7], v[6:7], v[136:137], v[10:11]
	v_pk_fma_f32 v[4:5], v[4:5], v[134:135], v[8:9]
	global_store_dwordx4 v[26:27], v[4:7], off offset:512
	global_load_dwordx4 v[4:7], v[24:25], off offset:576
	s_waitcnt vmcnt(0)
	v_pk_fma_f32 v[2:3], v[2:3], v[132:133], v[6:7]
	v_pk_fma_f32 v[0:1], v[0:1], v[130:131], v[4:5]
	global_store_dwordx4 v[26:27], v[0:3], off offset:576
	s_cbranch_scc1 .LBB0_1366
	s_andn2_b64 vcc, exec, s[6:7]
	s_branch .LBB0_1365

.LBB0_1786:
	v_mul_f32_e32 v141, 0xbfb8aa3b, v126
	v_exp_f32_e32 v141, v141
	v_lshl_add_u32 v96, s42, 8, v137
	v_lshl_or_b32 v132, s41, 7, v139
	v_ashrrev_i32_e32 v133, 31, v132
	v_add_f32_e32 v141, 1.0, v141
	v_rcp_f32_e32 v141, v141
	s_cmp_eq_u32 s40, s36
	v_mul_f32_e32 v126, v126, v141
	v_mul_f32_e32 v122, v126, v122
	v_mul_f32_e32 v126, 0xbfb8aa3b, v127
	v_exp_f32_e32 v126, v126
	s_nop 0
	v_add_f32_e32 v126, 1.0, v126
	v_rcp_f32_e32 v126, v126
	s_nop 0
	v_mul_f32_e32 v126, v127, v126
	v_mul_f32_e32 v123, v126, v123
	v_mul_f32_e32 v126, 0xbfb8aa3b, v128
	v_exp_f32_e32 v126, v126
	s_nop 0
	v_add_f32_e32 v126, 1.0, v126
	v_rcp_f32_e32 v126, v126
	s_nop 0
	v_mul_f32_e32 v126, v128, v126
	v_mul_f32_e32 v124, v126, v124
	v_mul_f32_e32 v126, 0xbfb8aa3b, v129
	v_exp_f32_e32 v126, v126
	s_nop 0
	v_add_f32_e32 v126, 1.0, v126
	v_rcp_f32_e32 v126, v126
	s_nop 0
	v_mul_f32_e32 v126, v129, v126
	v_mul_f32_e32 v125, v126, v125
	v_mul_f32_e32 v126, 0xbfb8aa3b, v118
	v_exp_f32_e32 v126, v126
	s_nop 0
	v_add_f32_e32 v126, 1.0, v126
	v_rcp_f32_e32 v126, v126
	s_nop 0
	v_mul_f32_e32 v118, v118, v126
	v_mul_f32_e32 v114, v118, v114
	v_mul_f32_e32 v118, 0xbfb8aa3b, v119
	v_exp_f32_e32 v118, v118
	s_nop 0
	v_add_f32_e32 v118, 1.0, v118
	v_rcp_f32_e32 v118, v118
	s_nop 0
	v_mul_f32_e32 v118, v119, v118
	v_mul_f32_e32 v115, v118, v115
	v_mul_f32_e32 v118, 0xbfb8aa3b, v120
	v_exp_f32_e32 v118, v118
	s_nop 0
	v_add_f32_e32 v118, 1.0, v118
	v_rcp_f32_e32 v118, v118
	s_nop 0
	v_mul_f32_e32 v118, v120, v118
	v_mul_f32_e32 v118, v118, v116
	v_mul_f32_e32 v116, 0xbfb8aa3b, v121
	v_exp_f32_e32 v116, v116
	s_nop 0
	v_add_f32_e32 v116, 1.0, v116
	v_rcp_f32_e32 v116, v116
	s_nop 0
	v_mul_f32_e32 v116, v121, v116
	v_mul_f32_e32 v119, v116, v117
	v_mov_b32_e32 v116, v97
	v_mov_b32_e32 v117, v97
	v_cvt_pk_fp8_f32 v116, v122, v123
	v_cvt_pk_fp8_f32 v117, v114, v115
	v_mov_b64_e32 v[114:115], s[6:7]
	v_cvt_pk_fp8_f32 v116, v124, v125 op_sel:[0,0,1]
	v_cvt_pk_fp8_f32 v117, v118, v119 op_sel:[0,0,1]
	v_mad_i64_i32 v[118:119], s[14:15], v96, s72, v[114:115]
	v_lshl_add_u64 v[118:119], v[118:119], 0, v[132:133]
	global_store_dwordx2 v[118:119], v[116:117], off
	v_mul_f32_e32 v116, 0xbfb8aa3b, v110
	v_exp_f32_e32 v116, v116
	s_nop 0
	v_add_f32_e32 v116, 1.0, v116
	v_rcp_f32_e32 v116, v116
	s_nop 0
	v_mul_f32_e32 v110, v110, v116
	v_mul_f32_e32 v106, v110, v106
	v_mul_f32_e32 v110, 0xbfb8aa3b, v111
	v_exp_f32_e32 v110, v110
	s_nop 0
	v_add_f32_e32 v110, 1.0, v110
	v_rcp_f32_e32 v110, v110
	s_nop 0
	v_mul_f32_e32 v110, v111, v110
	v_mul_f32_e32 v107, v110, v107
	v_mul_f32_e32 v110, 0xbfb8aa3b, v112
	v_exp_f32_e32 v110, v110
	s_nop 0
	v_add_f32_e32 v110, 1.0, v110
	v_rcp_f32_e32 v110, v110
	s_nop 0
	v_mul_f32_e32 v110, v112, v110
	v_mul_f32_e32 v108, v110, v108
	v_mul_f32_e32 v110, 0xbfb8aa3b, v113
	v_exp_f32_e32 v110, v110
	s_nop 0
	v_add_f32_e32 v110, 1.0, v110
	v_rcp_f32_e32 v110, v110
	s_nop 0
	v_mul_f32_e32 v110, v113, v110
	v_mul_f32_e32 v109, v110, v109
	v_mul_f32_e32 v110, 0xbfb8aa3b, v102
	v_exp_f32_e32 v110, v110
	s_nop 0
	v_add_f32_e32 v110, 1.0, v110
	v_rcp_f32_e32 v110, v110
	s_nop 0
	v_mul_f32_e32 v102, v102, v110
	v_mul_f32_e32 v102, v102, v98
	v_mul_f32_e32 v98, 0xbfb8aa3b, v103
	v_exp_f32_e32 v98, v98
	s_nop 0
	v_add_f32_e32 v98, 1.0, v98
	v_rcp_f32_e32 v98, v98
	s_nop 0
	v_mul_f32_e32 v98, v103, v98
	v_mul_f32_e32 v103, v98, v99
	v_mul_f32_e32 v98, 0xbfb8aa3b, v104
	v_exp_f32_e32 v98, v98
	v_mov_b32_e32 v99, v97
	v_cvt_pk_fp8_f32 v99, v102, v103
	v_add_f32_e32 v98, 1.0, v98
	v_rcp_f32_e32 v98, v98
	s_nop 0
	v_mul_f32_e32 v98, v104, v98
	v_mul_f32_e32 v100, v98, v100
	v_mul_f32_e32 v98, 0xbfb8aa3b, v105
	v_exp_f32_e32 v98, v98
	s_nop 0
	v_add_f32_e32 v98, 1.0, v98
	v_rcp_f32_e32 v98, v98
	s_nop 0
	v_mul_f32_e32 v98, v105, v98
	v_mul_f32_e32 v101, v98, v101
	v_mov_b32_e32 v98, v97
	v_cvt_pk_fp8_f32 v98, v106, v107
	v_cvt_pk_fp8_f32 v99, v100, v101 op_sel:[0,0,1]
	v_or_b32_e32 v100, 16, v96
	v_mad_i64_i32 v[100:101], s[14:15], v100, s72, v[114:115]
	v_cvt_pk_fp8_f32 v98, v108, v109 op_sel:[0,0,1]
	v_lshl_add_u64 v[100:101], v[100:101], 0, v[132:133]
	global_store_dwordx2 v[100:101], v[98:99], off
	v_mul_f32_e32 v98, 0xbfb8aa3b, v92
	v_exp_f32_e32 v98, v98
	s_nop 0
	v_add_f32_e32 v98, 1.0, v98
	v_rcp_f32_e32 v98, v98
	s_nop 0
	v_mul_f32_e32 v92, v92, v98
	v_mul_f32_e32 v88, v92, v88
	v_mul_f32_e32 v92, 0xbfb8aa3b, v93
	v_exp_f32_e32 v92, v92
	s_nop 0
	v_add_f32_e32 v92, 1.0, v92
	v_rcp_f32_e32 v92, v92
	s_nop 0
	v_mul_f32_e32 v92, v93, v92
	v_mul_f32_e32 v89, v92, v89
	v_mul_f32_e32 v92, 0xbfb8aa3b, v94
	v_exp_f32_e32 v92, v92
	s_nop 0
	v_add_f32_e32 v92, 1.0, v92
	v_rcp_f32_e32 v92, v92
	s_nop 0
	v_mul_f32_e32 v92, v94, v92
	v_mul_f32_e32 v90, v92, v90
	v_mul_f32_e32 v92, 0xbfb8aa3b, v95
	v_exp_f32_e32 v92, v92
	s_nop 0
	v_add_f32_e32 v92, 1.0, v92
	v_rcp_f32_e32 v92, v92
	s_nop 0
	v_mul_f32_e32 v92, v95, v92
	v_mul_f32_e32 v91, v92, v91
	v_mul_f32_e32 v92, 0xbfb8aa3b, v84
	v_exp_f32_e32 v92, v92
	s_nop 0
	v_add_f32_e32 v92, 1.0, v92
	v_rcp_f32_e32 v92, v92
	s_nop 0
	v_mul_f32_e32 v84, v84, v92
	v_mul_f32_e32 v84, v84, v80
	v_mul_f32_e32 v80, 0xbfb8aa3b, v85
	v_exp_f32_e32 v80, v80
	s_nop 0
	v_add_f32_e32 v80, 1.0, v80
	v_rcp_f32_e32 v80, v80
	s_nop 0
	v_mul_f32_e32 v80, v85, v80
	v_mul_f32_e32 v85, v80, v81
	v_mul_f32_e32 v80, 0xbfb8aa3b, v86
	v_exp_f32_e32 v80, v80
	v_mov_b32_e32 v81, v97
	v_cvt_pk_fp8_f32 v81, v84, v85
	v_add_f32_e32 v80, 1.0, v80
	v_rcp_f32_e32 v80, v80
	s_nop 0
	v_mul_f32_e32 v80, v86, v80
	v_mul_f32_e32 v82, v80, v82
	v_mul_f32_e32 v80, 0xbfb8aa3b, v87
	v_exp_f32_e32 v80, v80
	s_nop 0
	v_add_f32_e32 v80, 1.0, v80
	v_rcp_f32_e32 v80, v80
	s_nop 0
	v_mul_f32_e32 v80, v87, v80
	v_mul_f32_e32 v83, v80, v83
	v_mov_b32_e32 v80, v97
	v_cvt_pk_fp8_f32 v80, v88, v89
	v_cvt_pk_fp8_f32 v81, v82, v83 op_sel:[0,0,1]
	v_or_b32_e32 v82, 32, v96
	v_mad_i64_i32 v[82:83], s[14:15], v82, s72, v[114:115]
	v_cvt_pk_fp8_f32 v80, v90, v91 op_sel:[0,0,1]
	v_lshl_add_u64 v[82:83], v[82:83], 0, v[132:133]
	global_store_dwordx2 v[82:83], v[80:81], off
	v_mul_f32_e32 v80, 0xbfb8aa3b, v76
	v_exp_f32_e32 v80, v80
	s_nop 0
	v_add_f32_e32 v80, 1.0, v80
	v_rcp_f32_e32 v80, v80
	s_nop 0
	v_mul_f32_e32 v76, v76, v80
	v_mul_f32_e32 v72, v76, v72
	v_mul_f32_e32 v76, 0xbfb8aa3b, v77
	v_exp_f32_e32 v76, v76
	s_nop 0
	v_add_f32_e32 v76, 1.0, v76
	v_rcp_f32_e32 v76, v76
	s_nop 0
	v_mul_f32_e32 v76, v77, v76
	v_mul_f32_e32 v73, v76, v73
	v_mul_f32_e32 v76, 0xbfb8aa3b, v78
	v_exp_f32_e32 v76, v76
	s_nop 0
	v_add_f32_e32 v76, 1.0, v76
	v_rcp_f32_e32 v76, v76
	s_nop 0
	v_mul_f32_e32 v76, v78, v76
	v_mul_f32_e32 v74, v76, v74
	v_mul_f32_e32 v76, 0xbfb8aa3b, v79
	v_exp_f32_e32 v76, v76
	s_nop 0
	v_add_f32_e32 v76, 1.0, v76
	v_rcp_f32_e32 v76, v76
	s_nop 0
	v_mul_f32_e32 v76, v79, v76
	v_mul_f32_e32 v75, v76, v75
	v_mul_f32_e32 v76, 0xbfb8aa3b, v68
	v_exp_f32_e32 v76, v76
	s_nop 0
	v_add_f32_e32 v76, 1.0, v76
	v_rcp_f32_e32 v76, v76
	s_nop 0
	v_mul_f32_e32 v68, v68, v76
	v_mul_f32_e32 v68, v68, v64
	v_mul_f32_e32 v64, 0xbfb8aa3b, v69
	v_exp_f32_e32 v64, v64
	s_nop 0
	v_add_f32_e32 v64, 1.0, v64
	v_rcp_f32_e32 v64, v64
	s_nop 0
	v_mul_f32_e32 v64, v69, v64
	v_mul_f32_e32 v69, v64, v65
	v_mul_f32_e32 v64, 0xbfb8aa3b, v70
	v_exp_f32_e32 v64, v64
	v_mov_b32_e32 v65, v97
	v_cvt_pk_fp8_f32 v65, v68, v69
	v_add_f32_e32 v64, 1.0, v64
	v_rcp_f32_e32 v64, v64
	s_nop 0
	v_mul_f32_e32 v64, v70, v64
	v_mul_f32_e32 v66, v64, v66
	v_mul_f32_e32 v64, 0xbfb8aa3b, v71
	v_exp_f32_e32 v64, v64
	s_nop 0
	v_add_f32_e32 v64, 1.0, v64
	v_rcp_f32_e32 v64, v64
	s_nop 0
	v_mul_f32_e32 v64, v71, v64
	v_mul_f32_e32 v67, v64, v67
	v_mov_b32_e32 v64, v97
	v_cvt_pk_fp8_f32 v64, v72, v73
	v_cvt_pk_fp8_f32 v65, v66, v67 op_sel:[0,0,1]
	v_or_b32_e32 v66, 48, v96
	v_mad_i64_i32 v[66:67], s[14:15], v66, s72, v[114:115]
	v_cvt_pk_fp8_f32 v64, v74, v75 op_sel:[0,0,1]
	v_lshl_add_u64 v[66:67], v[66:67], 0, v[132:133]
	global_store_dwordx2 v[66:67], v[64:65], off
	v_mul_f32_e32 v65, 0xbfb8aa3b, v60
	v_exp_f32_e32 v65, v65
	v_add_u32_e32 v64, 0x80, v96
	v_add_f32_e32 v65, 1.0, v65
	v_rcp_f32_e32 v65, v65
	s_nop 0
	v_mul_f32_e32 v60, v60, v65
	v_mul_f32_e32 v56, v60, v56
	v_mul_f32_e32 v60, 0xbfb8aa3b, v61
	v_exp_f32_e32 v60, v60
	s_nop 0
	v_add_f32_e32 v60, 1.0, v60
	v_rcp_f32_e32 v60, v60
	s_nop 0
	v_mul_f32_e32 v60, v61, v60
	v_mul_f32_e32 v57, v60, v57
	v_mul_f32_e32 v60, 0xbfb8aa3b, v62
	v_exp_f32_e32 v60, v60
	s_nop 0
	v_add_f32_e32 v60, 1.0, v60
	v_rcp_f32_e32 v60, v60
	s_nop 0
	v_mul_f32_e32 v60, v62, v60
	v_mul_f32_e32 v58, v60, v58
	v_mul_f32_e32 v60, 0xbfb8aa3b, v63
	v_exp_f32_e32 v60, v60
	s_nop 0
	v_add_f32_e32 v60, 1.0, v60
	v_rcp_f32_e32 v60, v60
	s_nop 0
	v_mul_f32_e32 v60, v63, v60
	v_mul_f32_e32 v59, v60, v59
	v_mul_f32_e32 v60, 0xbfb8aa3b, v52
	v_exp_f32_e32 v60, v60
	s_nop 0
	v_add_f32_e32 v60, 1.0, v60
	v_rcp_f32_e32 v60, v60
	s_nop 0
	v_mul_f32_e32 v52, v52, v60
	v_mul_f32_e32 v52, v52, v48
	v_mul_f32_e32 v48, 0xbfb8aa3b, v53
	v_exp_f32_e32 v48, v48
	s_nop 0
	v_add_f32_e32 v48, 1.0, v48
	v_rcp_f32_e32 v48, v48
	s_nop 0
	v_mul_f32_e32 v48, v53, v48
	v_mul_f32_e32 v53, v48, v49
	v_mul_f32_e32 v48, 0xbfb8aa3b, v54
	v_exp_f32_e32 v48, v48
	v_mov_b32_e32 v49, v97
	v_cvt_pk_fp8_f32 v49, v52, v53
	v_add_f32_e32 v48, 1.0, v48
	v_rcp_f32_e32 v48, v48
	s_nop 0
	v_mul_f32_e32 v48, v54, v48
	v_mul_f32_e32 v50, v48, v50
	v_mul_f32_e32 v48, 0xbfb8aa3b, v55
	v_exp_f32_e32 v48, v48
	s_nop 0
	v_add_f32_e32 v48, 1.0, v48
	v_rcp_f32_e32 v48, v48
	s_nop 0
	v_mul_f32_e32 v48, v55, v48
	v_mul_f32_e32 v51, v48, v51
	v_mov_b32_e32 v48, v97
	v_cvt_pk_fp8_f32 v48, v56, v57
	v_cvt_pk_fp8_f32 v49, v50, v51 op_sel:[0,0,1]
	v_mad_i64_i32 v[50:51], s[14:15], v64, s72, v[114:115]
	v_cvt_pk_fp8_f32 v48, v58, v59 op_sel:[0,0,1]
	v_lshl_add_u64 v[50:51], v[50:51], 0, v[132:133]
	global_store_dwordx2 v[50:51], v[48:49], off
	v_mul_f32_e32 v48, 0xbfb8aa3b, v44
	v_exp_f32_e32 v48, v48
	s_nop 0
	v_add_f32_e32 v48, 1.0, v48
	v_rcp_f32_e32 v48, v48
	s_nop 0
	v_mul_f32_e32 v44, v44, v48
	v_mul_f32_e32 v40, v44, v40
	v_mul_f32_e32 v44, 0xbfb8aa3b, v45
	v_exp_f32_e32 v44, v44
	s_nop 0
	v_add_f32_e32 v44, 1.0, v44
	v_rcp_f32_e32 v44, v44
	s_nop 0
	v_mul_f32_e32 v44, v45, v44
	v_mul_f32_e32 v41, v44, v41
	v_mul_f32_e32 v44, 0xbfb8aa3b, v46
	v_exp_f32_e32 v44, v44
	s_nop 0
	v_add_f32_e32 v44, 1.0, v44
	v_rcp_f32_e32 v44, v44
	s_nop 0
	v_mul_f32_e32 v44, v46, v44
	v_mul_f32_e32 v42, v44, v42
	v_mul_f32_e32 v44, 0xbfb8aa3b, v47
	v_exp_f32_e32 v44, v44
	s_nop 0
	v_add_f32_e32 v44, 1.0, v44
	v_rcp_f32_e32 v44, v44
	s_nop 0
	v_mul_f32_e32 v44, v47, v44
	v_mul_f32_e32 v43, v44, v43
	v_mul_f32_e32 v44, 0xbfb8aa3b, v36
	v_exp_f32_e32 v44, v44
	s_nop 0
	v_add_f32_e32 v44, 1.0, v44
	v_rcp_f32_e32 v44, v44
	s_nop 0
	v_mul_f32_e32 v36, v36, v44
	v_mul_f32_e32 v36, v36, v32
	v_mul_f32_e32 v32, 0xbfb8aa3b, v37
	v_exp_f32_e32 v32, v32
	s_nop 0
	v_add_f32_e32 v32, 1.0, v32
	v_rcp_f32_e32 v32, v32
	s_nop 0
	v_mul_f32_e32 v32, v37, v32
	v_mul_f32_e32 v37, v32, v33
	v_mul_f32_e32 v32, 0xbfb8aa3b, v38
	v_exp_f32_e32 v32, v32
	v_mov_b32_e32 v33, v97
	v_cvt_pk_fp8_f32 v33, v36, v37
	v_add_f32_e32 v32, 1.0, v32
	v_rcp_f32_e32 v32, v32
	s_nop 0
	v_mul_f32_e32 v32, v38, v32
	v_mul_f32_e32 v34, v32, v34
	v_mul_f32_e32 v32, 0xbfb8aa3b, v39
	v_exp_f32_e32 v32, v32
	s_nop 0
	v_add_f32_e32 v32, 1.0, v32
	v_rcp_f32_e32 v32, v32
	s_nop 0
	v_mul_f32_e32 v32, v39, v32
	v_mul_f32_e32 v35, v32, v35
	v_mov_b32_e32 v32, v97
	v_cvt_pk_fp8_f32 v32, v40, v41
	v_cvt_pk_fp8_f32 v33, v34, v35 op_sel:[0,0,1]
	v_add_u32_e32 v34, 0x90, v96
	v_mad_i64_i32 v[34:35], s[14:15], v34, s72, v[114:115]
	v_cvt_pk_fp8_f32 v32, v42, v43 op_sel:[0,0,1]
	v_lshl_add_u64 v[34:35], v[34:35], 0, v[132:133]
	global_store_dwordx2 v[34:35], v[32:33], off
	v_mul_f32_e32 v32, 0xbfb8aa3b, v28
	v_exp_f32_e32 v32, v32
	s_nop 0
	v_add_f32_e32 v32, 1.0, v32
	v_rcp_f32_e32 v32, v32
	s_nop 0
	v_mul_f32_e32 v28, v28, v32
	v_mul_f32_e32 v24, v28, v24
	v_mul_f32_e32 v28, 0xbfb8aa3b, v29
	v_exp_f32_e32 v28, v28
	s_nop 0
	v_add_f32_e32 v28, 1.0, v28
	v_rcp_f32_e32 v28, v28
	s_nop 0
	v_mul_f32_e32 v28, v29, v28
	v_mul_f32_e32 v25, v28, v25
	v_mul_f32_e32 v28, 0xbfb8aa3b, v30
	v_exp_f32_e32 v28, v28
	s_nop 0
	v_add_f32_e32 v28, 1.0, v28
	v_rcp_f32_e32 v28, v28
	s_nop 0
	v_mul_f32_e32 v28, v30, v28
	v_mul_f32_e32 v26, v28, v26
	v_mul_f32_e32 v28, 0xbfb8aa3b, v31
	v_exp_f32_e32 v28, v28
	s_nop 0
	v_add_f32_e32 v28, 1.0, v28
	v_rcp_f32_e32 v28, v28
	s_nop 0
	v_mul_f32_e32 v28, v31, v28
	v_mul_f32_e32 v27, v28, v27
	v_mul_f32_e32 v28, 0xbfb8aa3b, v20
	v_exp_f32_e32 v28, v28
	s_nop 0
	v_add_f32_e32 v28, 1.0, v28
	v_rcp_f32_e32 v28, v28
	s_nop 0
	v_mul_f32_e32 v20, v20, v28
	v_mul_f32_e32 v20, v20, v16
	v_mul_f32_e32 v16, 0xbfb8aa3b, v21
	v_exp_f32_e32 v16, v16
	s_nop 0
	v_add_f32_e32 v16, 1.0, v16
	v_rcp_f32_e32 v16, v16
	s_nop 0
	v_mul_f32_e32 v16, v21, v16
	v_mul_f32_e32 v21, v16, v17
	v_mul_f32_e32 v16, 0xbfb8aa3b, v22
	v_exp_f32_e32 v16, v16
	v_mov_b32_e32 v17, v97
	v_cvt_pk_fp8_f32 v17, v20, v21
	v_add_f32_e32 v16, 1.0, v16
	v_rcp_f32_e32 v16, v16
	s_nop 0
	v_mul_f32_e32 v16, v22, v16
	v_mul_f32_e32 v18, v16, v18
	v_mul_f32_e32 v16, 0xbfb8aa3b, v23
	v_exp_f32_e32 v16, v16
	s_nop 0
	v_add_f32_e32 v16, 1.0, v16
	v_rcp_f32_e32 v16, v16
	s_nop 0
	v_mul_f32_e32 v16, v23, v16
	v_mul_f32_e32 v19, v16, v19
	v_mov_b32_e32 v16, v97
	v_cvt_pk_fp8_f32 v16, v24, v25
	v_cvt_pk_fp8_f32 v17, v18, v19 op_sel:[0,0,1]
	v_add_u32_e32 v18, 0xa0, v96
	v_mad_i64_i32 v[18:19], s[14:15], v18, s72, v[114:115]
	v_cvt_pk_fp8_f32 v16, v26, v27 op_sel:[0,0,1]
	v_lshl_add_u64 v[18:19], v[18:19], 0, v[132:133]
	global_store_dwordx2 v[18:19], v[16:17], off
	v_mul_f32_e32 v16, 0xbfb8aa3b, v12
	v_exp_f32_e32 v16, v16
	s_nop 0
	v_add_f32_e32 v16, 1.0, v16
	v_rcp_f32_e32 v16, v16
	s_nop 0
	v_mul_f32_e32 v12, v12, v16
	v_mul_f32_e32 v8, v12, v8
	v_mul_f32_e32 v12, 0xbfb8aa3b, v13
	v_exp_f32_e32 v12, v12
	s_nop 0
	v_add_f32_e32 v12, 1.0, v12
	v_rcp_f32_e32 v12, v12
	s_nop 0
	v_mul_f32_e32 v12, v13, v12
	v_mul_f32_e32 v9, v12, v9
	v_mul_f32_e32 v12, 0xbfb8aa3b, v14
	v_exp_f32_e32 v12, v12
	s_nop 0
	v_add_f32_e32 v12, 1.0, v12
	v_rcp_f32_e32 v12, v12
	s_nop 0
	v_mul_f32_e32 v12, v14, v12
	v_mul_f32_e32 v10, v12, v10
	v_mul_f32_e32 v12, 0xbfb8aa3b, v15
	v_exp_f32_e32 v12, v12
	s_nop 0
	v_add_f32_e32 v12, 1.0, v12
	v_rcp_f32_e32 v12, v12
	s_nop 0
	v_mul_f32_e32 v12, v15, v12
	v_mul_f32_e32 v11, v12, v11
	v_mul_f32_e32 v12, 0xbfb8aa3b, v4
	v_exp_f32_e32 v12, v12
	s_nop 0
	v_add_f32_e32 v12, 1.0, v12
	v_rcp_f32_e32 v12, v12
	s_nop 0
	v_mul_f32_e32 v4, v4, v12
	v_mul_f32_e32 v4, v4, v0
	v_mul_f32_e32 v0, 0xbfb8aa3b, v5
	v_exp_f32_e32 v0, v0
	s_nop 0
	v_add_f32_e32 v0, 1.0, v0
	v_rcp_f32_e32 v0, v0
	s_nop 0
	v_mul_f32_e32 v0, v5, v0
	v_mul_f32_e32 v5, v0, v1
	v_mul_f32_e32 v0, 0xbfb8aa3b, v6
	v_exp_f32_e32 v0, v0
	v_mov_b32_e32 v1, v97
	v_cvt_pk_fp8_f32 v1, v4, v5
	v_add_f32_e32 v0, 1.0, v0
	v_rcp_f32_e32 v0, v0
	s_nop 0
	v_mul_f32_e32 v0, v6, v0
	v_mul_f32_e32 v2, v0, v2
	v_mul_f32_e32 v0, 0xbfb8aa3b, v7
	v_exp_f32_e32 v0, v0
	s_nop 0
	v_add_f32_e32 v0, 1.0, v0
	v_rcp_f32_e32 v0, v0
	s_nop 0
	v_mul_f32_e32 v0, v7, v0
	v_mul_f32_e32 v3, v0, v3
	v_mov_b32_e32 v0, v97
	v_cvt_pk_fp8_f32 v0, v8, v9
	v_cvt_pk_fp8_f32 v1, v2, v3 op_sel:[0,0,1]
	v_add_u32_e32 v2, 0xb0, v96
	v_mad_i64_i32 v[2:3], s[14:15], v2, s72, v[114:115]
	v_cvt_pk_fp8_f32 v0, v10, v11 op_sel:[0,0,1]
	v_lshl_add_u64 v[2:3], v[2:3], 0, v[132:133]
	s_mov_b64 s[14:15], -1
	global_store_dwordx2 v[2:3], v[0:1], off
	s_cbranch_scc1 .LBB0_1779
	s_andn2_b64 vcc, exec, s[2:3]
	s_branch .LBB0_1778

.Lmy_peel1956_exit:
	s_cmp_lg_u32 s43, s39
	s_cbranch_scc1 .LBB0_1959
	s_and_b64 vcc, exec, s[10:11]
	s_cbranch_vccz .LBB0_1959
	s_barrier
.LBB0_1959:
	s_lshl_b32 s20, s47, 8
	s_min_i32 s18, s20, 0x2000
	s_ashr_i32 s18, s18, 11
	v_lshl_or_b32 v132, s46, 8, v157
	s_mul_hi_i32 s19, s18, 0xc000
	s_mul_i32 s18, s18, 0xc000
	s_add_u32 s18, s55, s18
	v_ashrrev_i32_e32 v133, 31, v132
	s_addc_u32 s19, s69, s19
	v_lshlrev_b64 v[150:151], 2, v[132:133]
	v_lshl_add_u64 v[132:133], s[18:19], 0, v[150:151]
	s_mov_b64 s[18:19], 0xa000
	v_lshl_add_u64 v[148:149], v[132:133], 0, s[18:19]
	s_mov_b32 s18, 0xa000
	v_add_co_u32_e32 v132, vcc, s18, v132
	global_load_dwordx4 v[160:163], v[148:149], off offset:576
	s_nop 0
	v_addc_co_u32_e32 v133, vcc, 0, v133, vcc
	global_load_dwordx4 v[132:135], v[132:133], off
	v_add_u32_e32 v152, s20, v155
	v_ashrrev_i32_e32 v153, 31, v152
	s_mov_b64 s[18:19], 0x100000
	s_cmp_eq_u32 s43, s39
	s_waitcnt vmcnt(0)
	v_pk_mul_f32 v[144:145], v[134:135], s[58:59] op_sel_hi:[1,0]
	v_pk_mul_f32 v[146:147], v[132:133], s[58:59] op_sel_hi:[1,0]
	global_load_dwordx4 v[132:135], v[148:149], off offset:64
	s_waitcnt vmcnt(0)
	v_pk_mul_f32 v[140:141], v[134:135], s[58:59] op_sel_hi:[1,0]
	v_pk_mul_f32 v[142:143], v[132:133], s[58:59] op_sel_hi:[1,0]
	global_load_dwordx4 v[132:135], v[148:149], off offset:512
	v_lshlrev_b64 v[148:149], 13, v[152:153]
	v_lshl_add_u64 v[148:149], s[8:9], 0, v[148:149]
	v_lshl_add_u64 v[148:149], v[148:149], 0, v[150:151]
	s_waitcnt vmcnt(0)
	v_pk_mul_f32 v[136:137], v[134:135], s[58:59] op_sel_hi:[1,0]
	v_pk_mul_f32 v[138:139], v[132:133], s[58:59] op_sel_hi:[1,0]
	v_pk_mul_f32 v[132:133], v[162:163], s[58:59] op_sel_hi:[1,0]
	v_pk_mul_f32 v[134:135], v[160:161], s[58:59] op_sel_hi:[1,0]
	global_load_dwordx4 v[160:163], v[148:149], off
	s_waitcnt vmcnt(0)
	v_pk_fma_f32 v[128:129], v[128:129], v[144:145], v[162:163]
	v_pk_fma_f32 v[126:127], v[126:127], v[146:147], v[160:161]
	global_store_dwordx4 v[148:149], v[126:129], off
	global_load_dwordx4 v[126:129], v[148:149], off offset:64
	s_waitcnt vmcnt(0)
	v_pk_fma_f32 v[124:125], v[124:125], v[140:141], v[128:129]
	v_pk_fma_f32 v[122:123], v[122:123], v[142:143], v[126:127]
	global_store_dwordx4 v[148:149], v[122:125], off offset:64
	global_load_dwordx4 v[122:125], v[148:149], off offset:512
	s_waitcnt vmcnt(0)
	v_pk_fma_f32 v[120:121], v[120:121], v[136:137], v[124:125]
	v_pk_fma_f32 v[118:119], v[118:119], v[138:139], v[122:123]
	global_store_dwordx4 v[148:149], v[118:121], off offset:512
	global_load_dwordx4 v[118:121], v[148:149], off offset:576
	s_waitcnt vmcnt(0)
	v_pk_fma_f32 v[116:117], v[116:117], v[132:133], v[120:121]
	v_pk_fma_f32 v[114:115], v[114:115], v[134:135], v[118:119]
	global_store_dwordx4 v[148:149], v[114:117], off offset:576
	s_nop 1
	v_or_b32_e32 v114, 16, v152
	v_ashrrev_i32_e32 v115, 31, v114
	v_lshlrev_b64 v[114:115], 13, v[114:115]
	v_lshl_add_u64 v[114:115], s[8:9], 0, v[114:115]
	v_lshl_add_u64 v[118:119], v[114:115], 0, v[150:151]
	global_load_dwordx4 v[114:117], v[118:119], off
	s_waitcnt vmcnt(0)
	v_pk_fma_f32 v[112:113], v[112:113], v[144:145], v[116:117]
	v_pk_fma_f32 v[110:111], v[110:111], v[146:147], v[114:115]
	global_store_dwordx4 v[118:119], v[110:113], off
	global_load_dwordx4 v[110:113], v[118:119], off offset:64
	s_waitcnt vmcnt(0)
	v_pk_fma_f32 v[108:109], v[108:109], v[140:141], v[112:113]
	v_pk_fma_f32 v[106:107], v[106:107], v[142:143], v[110:111]
	global_store_dwordx4 v[118:119], v[106:109], off offset:64
	global_load_dwordx4 v[106:109], v[118:119], off offset:512
	s_waitcnt vmcnt(0)
	v_pk_fma_f32 v[104:105], v[104:105], v[136:137], v[108:109]
	v_pk_fma_f32 v[102:103], v[102:103], v[138:139], v[106:107]
	global_store_dwordx4 v[118:119], v[102:105], off offset:512
	global_load_dwordx4 v[102:105], v[118:119], off offset:576
	s_waitcnt vmcnt(0)
	v_pk_fma_f32 v[100:101], v[100:101], v[132:133], v[104:105]
	v_pk_fma_f32 v[98:99], v[98:99], v[134:135], v[102:103]
	global_store_dwordx4 v[118:119], v[98:101], off offset:576
	s_nop 1
	v_or_b32_e32 v98, 32, v152
	v_ashrrev_i32_e32 v99, 31, v98
	v_lshlrev_b64 v[98:99], 13, v[98:99]
	v_lshl_add_u64 v[98:99], s[8:9], 0, v[98:99]
	v_lshl_add_u64 v[102:103], v[98:99], 0, v[150:151]
	global_load_dwordx4 v[98:101], v[102:103], off
	s_waitcnt vmcnt(0)
	v_pk_fma_f32 v[94:95], v[94:95], v[144:145], v[100:101]
	v_pk_fma_f32 v[92:93], v[92:93], v[146:147], v[98:99]
	global_store_dwordx4 v[102:103], v[92:95], off
	global_load_dwordx4 v[92:95], v[102:103], off offset:64
	s_waitcnt vmcnt(0)
	v_pk_fma_f32 v[90:91], v[90:91], v[140:141], v[94:95]
	v_pk_fma_f32 v[88:89], v[88:89], v[142:143], v[92:93]
	global_store_dwordx4 v[102:103], v[88:91], off offset:64
	global_load_dwordx4 v[88:91], v[102:103], off offset:512
	s_waitcnt vmcnt(0)
	v_pk_fma_f32 v[86:87], v[86:87], v[136:137], v[90:91]
	v_pk_fma_f32 v[84:85], v[84:85], v[138:139], v[88:89]
	global_store_dwordx4 v[102:103], v[84:87], off offset:512
	global_load_dwordx4 v[84:87], v[102:103], off offset:576
	s_waitcnt vmcnt(0)
	v_pk_fma_f32 v[82:83], v[82:83], v[132:133], v[86:87]
	v_pk_fma_f32 v[80:81], v[80:81], v[134:135], v[84:85]
	global_store_dwordx4 v[102:103], v[80:83], off offset:576
	s_nop 1
	v_or_b32_e32 v80, 48, v152
	v_ashrrev_i32_e32 v81, 31, v80
	v_lshlrev_b64 v[80:81], 13, v[80:81]
	v_lshl_add_u64 v[80:81], s[8:9], 0, v[80:81]
	v_lshl_add_u64 v[84:85], v[80:81], 0, v[150:151]
	global_load_dwordx4 v[80:83], v[84:85], off
	s_waitcnt vmcnt(0)
	v_pk_fma_f32 v[78:79], v[78:79], v[144:145], v[82:83]
	v_pk_fma_f32 v[76:77], v[76:77], v[146:147], v[80:81]
	global_store_dwordx4 v[84:85], v[76:79], off
	global_load_dwordx4 v[76:79], v[84:85], off offset:64
	s_waitcnt vmcnt(0)
	v_pk_fma_f32 v[74:75], v[74:75], v[140:141], v[78:79]
	v_pk_fma_f32 v[72:73], v[72:73], v[142:143], v[76:77]
	global_store_dwordx4 v[84:85], v[72:75], off offset:64
	global_load_dwordx4 v[72:75], v[84:85], off offset:512
	s_waitcnt vmcnt(0)
	v_pk_fma_f32 v[70:71], v[70:71], v[136:137], v[74:75]
	v_pk_fma_f32 v[68:69], v[68:69], v[138:139], v[72:73]
	global_store_dwordx4 v[84:85], v[68:71], off offset:512
	global_load_dwordx4 v[68:71], v[84:85], off offset:576
	s_waitcnt vmcnt(0)
	v_pk_fma_f32 v[66:67], v[66:67], v[132:133], v[70:71]
	v_add_co_u32_e32 v70, vcc, s85, v148
	v_pk_fma_f32 v[64:65], v[64:65], v[134:135], v[68:69]
	s_nop 0
	v_addc_co_u32_e32 v71, vcc, 0, v149, vcc
	global_store_dwordx4 v[84:85], v[64:67], off offset:576
	global_load_dwordx4 v[64:67], v[70:71], off
	v_lshl_add_u64 v[68:69], v[148:149], 0, s[18:19]
	s_mov_b64 s[18:19], 0x120000
	s_waitcnt vmcnt(0)
	v_pk_fma_f32 v[62:63], v[62:63], v[144:145], v[66:67]
	v_pk_fma_f32 v[60:61], v[60:61], v[146:147], v[64:65]
	global_store_dwordx4 v[70:71], v[60:63], off
	global_load_dwordx4 v[60:63], v[68:69], off offset:64
	s_waitcnt vmcnt(0)
	v_pk_fma_f32 v[58:59], v[58:59], v[140:141], v[62:63]
	v_pk_fma_f32 v[56:57], v[56:57], v[142:143], v[60:61]
	global_store_dwordx4 v[68:69], v[56:59], off offset:64
	global_load_dwordx4 v[56:59], v[68:69], off offset:512
	s_waitcnt vmcnt(0)
	v_pk_fma_f32 v[54:55], v[54:55], v[136:137], v[58:59]
	v_pk_fma_f32 v[52:53], v[52:53], v[138:139], v[56:57]
	global_store_dwordx4 v[68:69], v[52:55], off offset:512
	global_load_dwordx4 v[52:55], v[68:69], off offset:576
	s_waitcnt vmcnt(0)
	v_pk_fma_f32 v[50:51], v[50:51], v[132:133], v[54:55]
	v_add_co_u32_e32 v54, vcc, s86, v148
	v_pk_fma_f32 v[48:49], v[48:49], v[134:135], v[52:53]
	s_nop 0
	v_addc_co_u32_e32 v55, vcc, 0, v149, vcc
	global_store_dwordx4 v[68:69], v[48:51], off offset:576
	global_load_dwordx4 v[50:53], v[54:55], off
	s_waitcnt vmcnt(0)
	v_pk_fma_f32 v[46:47], v[46:47], v[144:145], v[52:53]
	v_lshl_add_u64 v[48:49], v[148:149], 0, s[18:19]
	v_pk_fma_f32 v[44:45], v[44:45], v[146:147], v[50:51]
	global_store_dwordx4 v[54:55], v[44:47], off
	global_load_dwordx4 v[44:47], v[48:49], off offset:64
	s_mov_b64 s[18:19], 0x140000
	s_waitcnt vmcnt(0)
	v_pk_fma_f32 v[42:43], v[42:43], v[140:141], v[46:47]
	v_pk_fma_f32 v[40:41], v[40:41], v[142:143], v[44:45]
	global_store_dwordx4 v[48:49], v[40:43], off offset:64
	global_load_dwordx4 v[40:43], v[48:49], off offset:512
	s_waitcnt vmcnt(0)
	v_pk_fma_f32 v[38:39], v[38:39], v[136:137], v[42:43]
	v_pk_fma_f32 v[36:37], v[36:37], v[138:139], v[40:41]
	global_store_dwordx4 v[48:49], v[36:39], off offset:512
	global_load_dwordx4 v[36:39], v[48:49], off offset:576
	s_waitcnt vmcnt(0)
	v_pk_fma_f32 v[32:33], v[32:33], v[134:135], v[36:37]
	v_lshl_add_u64 v[36:37], v[148:149], 0, s[18:19]
	s_mov_b32 s18, 0x140000
	v_pk_fma_f32 v[34:35], v[34:35], v[132:133], v[38:39]
	v_add_co_u32_e32 v38, vcc, s18, v148
	global_store_dwordx4 v[48:49], v[32:35], off offset:576
	s_nop 0
	v_addc_co_u32_e32 v39, vcc, 0, v149, vcc
	global_load_dwordx4 v[32:35], v[38:39], off
	s_mov_b64 s[18:19], 0x160000
	s_waitcnt vmcnt(0)
	v_pk_fma_f32 v[30:31], v[30:31], v[144:145], v[34:35]
	v_pk_fma_f32 v[28:29], v[28:29], v[146:147], v[32:33]
	global_store_dwordx4 v[38:39], v[28:31], off
	global_load_dwordx4 v[28:31], v[36:37], off offset:64
	s_waitcnt vmcnt(0)
	v_pk_fma_f32 v[26:27], v[26:27], v[140:141], v[30:31]
	v_pk_fma_f32 v[24:25], v[24:25], v[142:143], v[28:29]
	global_store_dwordx4 v[36:37], v[24:27], off offset:64
	global_load_dwordx4 v[24:27], v[36:37], off offset:512
	s_waitcnt vmcnt(0)
	v_pk_fma_f32 v[22:23], v[22:23], v[136:137], v[26:27]
	v_pk_fma_f32 v[20:21], v[20:21], v[138:139], v[24:25]
	global_store_dwordx4 v[36:37], v[20:23], off offset:512
	global_load_dwordx4 v[20:23], v[36:37], off offset:576
	s_waitcnt vmcnt(0)
	v_pk_fma_f32 v[18:19], v[18:19], v[132:133], v[22:23]
	v_add_co_u32_e32 v22, vcc, s84, v148
	v_pk_fma_f32 v[16:17], v[16:17], v[134:135], v[20:21]
	s_nop 0
	v_addc_co_u32_e32 v23, vcc, 0, v149, vcc
	global_store_dwordx4 v[36:37], v[16:19], off offset:576
	global_load_dwordx4 v[18:21], v[22:23], off
	s_waitcnt vmcnt(0)
	v_pk_fma_f32 v[14:15], v[14:15], v[144:145], v[20:21]
	v_lshl_add_u64 v[16:17], v[148:149], 0, s[18:19]
	v_pk_fma_f32 v[12:13], v[12:13], v[146:147], v[18:19]
	global_store_dwordx4 v[22:23], v[12:15], off
	global_load_dwordx4 v[12:15], v[16:17], off offset:64
	s_mov_b64 s[18:19], -1
	s_waitcnt vmcnt(0)
	v_pk_fma_f32 v[10:11], v[10:11], v[140:141], v[14:15]
	v_pk_fma_f32 v[8:9], v[8:9], v[142:143], v[12:13]
	global_store_dwordx4 v[16:17], v[8:11], off offset:64
	global_load_dwordx4 v[8:11], v[16:17], off offset:512
	s_waitcnt vmcnt(0)
	v_pk_fma_f32 v[6:7], v[6:7], v[136:137], v[10:11]
	v_pk_fma_f32 v[4:5], v[4:5], v[138:139], v[8:9]
	global_store_dwordx4 v[16:17], v[4:7], off offset:512
	global_load_dwordx4 v[4:7], v[16:17], off offset:576
	s_waitcnt vmcnt(0)
	v_pk_fma_f32 v[2:3], v[2:3], v[132:133], v[6:7]
	v_pk_fma_f32 v[0:1], v[0:1], v[134:135], v[4:5]
	global_store_dwordx4 v[16:17], v[0:3], off offset:576
	s_cbranch_scc1 .LBB0_1952
	s_andn2_b64 vcc, exec, s[2:3]
	s_branch .LBB0_1951

.Lmy_peel2129_exit:
	s_cmp_lg_u32 s36, s30
	s_cbranch_scc1 .LBB0_2132
	s_and_b64 vcc, exec, s[6:7]
	s_cbranch_vccz .LBB0_2132
	s_barrier
.LBB0_2132:
	v_mov_b32_e32 v140, v126
	v_mov_b32_e32 v141, v122
	v_pk_mul_f32 v[140:141], v[140:141], s[58:59] op_sel_hi:[1,0]
	v_lshl_add_u32 v96, s38, 8, v136
	v_mul_f32_e32 v122, 0xbfb8aa3b, v140
	v_exp_f32_e32 v122, v122
	v_lshl_or_b32 v130, s37, 7, v138
	v_ashrrev_i32_e32 v131, 31, v130
	s_cmp_eq_u32 s36, s30
	v_add_f32_e32 v122, 1.0, v122
	v_rcp_f32_e32 v122, v122
	s_nop 0
	v_mul_f32_e32 v122, v140, v122
	v_mul_f32_e32 v126, v122, v141
	v_mov_b32_e32 v122, v127
	v_pk_mul_f32 v[122:123], v[122:123], s[58:59] op_sel_hi:[1,0]
	s_nop 0
	v_mul_f32_e32 v127, 0xbfb8aa3b, v122
	v_exp_f32_e32 v127, v127
	s_nop 0
	v_add_f32_e32 v127, 1.0, v127
	v_rcp_f32_e32 v127, v127
	s_nop 0
	v_mul_f32_e32 v122, v122, v127
	v_mul_f32_e32 v127, v122, v123
	v_mov_b32_e32 v122, v128
	v_mov_b32_e32 v123, v124
	v_pk_mul_f32 v[122:123], v[122:123], s[58:59] op_sel_hi:[1,0]
	s_nop 0
	v_mul_f32_e32 v124, 0xbfb8aa3b, v122
	v_exp_f32_e32 v124, v124
	s_nop 0
	v_add_f32_e32 v124, 1.0, v124
	v_rcp_f32_e32 v124, v124
	s_nop 0
	v_mul_f32_e32 v122, v122, v124
	v_mov_b32_e32 v124, v129
	v_mul_f32_e32 v128, v122, v123
	v_pk_mul_f32 v[122:123], v[124:125], s[58:59] op_sel_hi:[1,0]
	s_nop 0
	v_mul_f32_e32 v124, 0xbfb8aa3b, v122
	v_exp_f32_e32 v124, v124
	s_nop 0
	v_add_f32_e32 v124, 1.0, v124
	v_rcp_f32_e32 v124, v124
	s_nop 0
	v_mul_f32_e32 v122, v122, v124
	v_mul_f32_e32 v124, v122, v123
	v_mov_b32_e32 v122, v118
	v_mov_b32_e32 v123, v114
	v_pk_mul_f32 v[122:123], v[122:123], s[58:59] op_sel_hi:[1,0]
	s_nop 0
	v_mul_f32_e32 v114, 0xbfb8aa3b, v122
	v_exp_f32_e32 v114, v114
	s_nop 0
	v_add_f32_e32 v114, 1.0, v114
	v_rcp_f32_e32 v114, v114
	s_nop 0
	v_mul_f32_e32 v114, v122, v114
	v_mul_f32_e32 v118, v114, v123
	v_mov_b32_e32 v114, v119
	v_pk_mul_f32 v[114:115], v[114:115], s[58:59] op_sel_hi:[1,0]
	s_nop 0
	v_mul_f32_e32 v119, 0xbfb8aa3b, v114
	v_exp_f32_e32 v119, v119
	s_nop 0
	v_add_f32_e32 v119, 1.0, v119
	v_rcp_f32_e32 v119, v119
	s_nop 0
	v_mul_f32_e32 v114, v114, v119
	v_mul_f32_e32 v119, v114, v115
	v_mov_b32_e32 v114, v120
	v_mov_b32_e32 v115, v116
	v_pk_mul_f32 v[114:115], v[114:115], s[58:59] op_sel_hi:[1,0]
	s_nop 0
	v_mul_f32_e32 v116, 0xbfb8aa3b, v114
	v_exp_f32_e32 v116, v116
	s_nop 0
	v_add_f32_e32 v116, 1.0, v116
	v_rcp_f32_e32 v116, v116
	s_nop 0
	v_mul_f32_e32 v114, v114, v116
	v_mov_b32_e32 v116, v121
	v_mul_f32_e32 v120, v114, v115
	v_pk_mul_f32 v[114:115], v[116:117], s[58:59] op_sel_hi:[1,0]
	v_mov_b32_e32 v117, v97
	v_mul_f32_e32 v116, 0xbfb8aa3b, v114
	v_exp_f32_e32 v116, v116
	v_cvt_pk_fp8_f32 v117, v118, v119
	v_add_f32_e32 v116, 1.0, v116
	v_rcp_f32_e32 v116, v116
	s_nop 0
	v_mul_f32_e32 v114, v114, v116
	v_mov_b32_e32 v116, v97
	v_cvt_pk_fp8_f32 v116, v126, v127
	v_mul_f32_e32 v114, v114, v115
	v_cvt_pk_fp8_f32 v117, v120, v114 op_sel:[0,0,1]
	v_mov_b64_e32 v[114:115], s[4:5]
	v_cvt_pk_fp8_f32 v116, v128, v124 op_sel:[0,0,1]
	v_mad_i64_i32 v[118:119], s[12:13], v96, s72, v[114:115]
	v_lshl_add_u64 v[118:119], v[118:119], 0, v[130:131]
	global_store_dwordx2 v[118:119], v[116:117], off
	v_mov_b32_e32 v116, v110
	v_mov_b32_e32 v117, v106
	v_pk_mul_f32 v[116:117], v[116:117], s[58:59] op_sel_hi:[1,0]
	s_nop 0
	v_mul_f32_e32 v106, 0xbfb8aa3b, v116
	v_exp_f32_e32 v106, v106
	s_nop 0
	v_add_f32_e32 v106, 1.0, v106
	v_rcp_f32_e32 v106, v106
	s_nop 0
	v_mul_f32_e32 v106, v116, v106
	v_mul_f32_e32 v110, v106, v117
	v_mov_b32_e32 v106, v111
	v_pk_mul_f32 v[106:107], v[106:107], s[58:59] op_sel_hi:[1,0]
	s_nop 0
	v_mul_f32_e32 v111, 0xbfb8aa3b, v106
	v_exp_f32_e32 v111, v111
	s_nop 0
	v_add_f32_e32 v111, 1.0, v111
	v_rcp_f32_e32 v111, v111
	s_nop 0
	v_mul_f32_e32 v106, v106, v111
	v_mul_f32_e32 v111, v106, v107
	v_mov_b32_e32 v106, v112
	v_mov_b32_e32 v107, v108
	v_pk_mul_f32 v[106:107], v[106:107], s[58:59] op_sel_hi:[1,0]
	s_nop 0
	v_mul_f32_e32 v108, 0xbfb8aa3b, v106
	v_exp_f32_e32 v108, v108
	s_nop 0
	v_add_f32_e32 v108, 1.0, v108
	v_rcp_f32_e32 v108, v108
	s_nop 0
	v_mul_f32_e32 v106, v106, v108
	v_mov_b32_e32 v108, v113
	v_mul_f32_e32 v112, v106, v107
	v_pk_mul_f32 v[106:107], v[108:109], s[58:59] op_sel_hi:[1,0]
	s_nop 0
	v_mul_f32_e32 v108, 0xbfb8aa3b, v106
	v_exp_f32_e32 v108, v108
	s_nop 0
	v_add_f32_e32 v108, 1.0, v108
	v_rcp_f32_e32 v108, v108
	s_nop 0
	v_mul_f32_e32 v106, v106, v108
	v_mul_f32_e32 v108, v106, v107
	v_mov_b32_e32 v106, v102
	v_mov_b32_e32 v107, v98
	v_pk_mul_f32 v[106:107], v[106:107], s[58:59] op_sel_hi:[1,0]
	s_nop 0
	v_mul_f32_e32 v98, 0xbfb8aa3b, v106
	v_exp_f32_e32 v98, v98
	s_nop 0
	v_add_f32_e32 v98, 1.0, v98
	v_rcp_f32_e32 v98, v98
	s_nop 0
	v_mul_f32_e32 v98, v106, v98
	v_mul_f32_e32 v102, v98, v107
	v_mov_b32_e32 v98, v103
	v_pk_mul_f32 v[98:99], v[98:99], s[58:59] op_sel_hi:[1,0]
	s_nop 0
	v_mul_f32_e32 v103, 0xbfb8aa3b, v98
	v_exp_f32_e32 v103, v103
	s_nop 0
	v_add_f32_e32 v103, 1.0, v103
	v_rcp_f32_e32 v103, v103
	s_nop 0
	v_mul_f32_e32 v98, v98, v103
	v_mul_f32_e32 v103, v98, v99
	v_mov_b32_e32 v98, v104
	v_mov_b32_e32 v99, v100
	v_pk_mul_f32 v[98:99], v[98:99], s[58:59] op_sel_hi:[1,0]
	s_nop 0
	v_mul_f32_e32 v100, 0xbfb8aa3b, v98
	v_exp_f32_e32 v100, v100
	s_nop 0
	v_add_f32_e32 v100, 1.0, v100
	v_rcp_f32_e32 v100, v100
	s_nop 0
	v_mul_f32_e32 v98, v98, v100
	v_mov_b32_e32 v100, v105
	v_mul_f32_e32 v104, v98, v99
	v_pk_mul_f32 v[98:99], v[100:101], s[58:59] op_sel_hi:[1,0]
	s_nop 0
	v_mul_f32_e32 v100, 0xbfb8aa3b, v98
	v_exp_f32_e32 v100, v100
	s_nop 0
	v_add_f32_e32 v100, 1.0, v100
	v_rcp_f32_e32 v100, v100
	s_nop 0
	v_mul_f32_e32 v98, v98, v100
	v_mul_f32_e32 v100, v98, v99
	v_mov_b32_e32 v98, v97
	v_mov_b32_e32 v99, v97
	v_cvt_pk_fp8_f32 v98, v110, v111
	v_cvt_pk_fp8_f32 v99, v102, v103
	v_cvt_pk_fp8_f32 v98, v112, v108 op_sel:[0,0,1]
	v_cvt_pk_fp8_f32 v99, v104, v100 op_sel:[0,0,1]
	v_or_b32_e32 v100, 16, v96
	v_mad_i64_i32 v[100:101], s[12:13], v100, s72, v[114:115]
	v_lshl_add_u64 v[100:101], v[100:101], 0, v[130:131]
	global_store_dwordx2 v[100:101], v[98:99], off
	v_mov_b32_e32 v98, v92
	v_mov_b32_e32 v99, v88
	v_pk_mul_f32 v[98:99], v[98:99], s[58:59] op_sel_hi:[1,0]
	s_nop 0
	v_mul_f32_e32 v88, 0xbfb8aa3b, v98
	v_exp_f32_e32 v88, v88
	s_nop 0
	v_add_f32_e32 v88, 1.0, v88
	v_rcp_f32_e32 v88, v88
	s_nop 0
	v_mul_f32_e32 v88, v98, v88
	v_mul_f32_e32 v92, v88, v99
	v_mov_b32_e32 v88, v93
	v_pk_mul_f32 v[88:89], v[88:89], s[58:59] op_sel_hi:[1,0]
	s_nop 0
	v_mul_f32_e32 v93, 0xbfb8aa3b, v88
	v_exp_f32_e32 v93, v93
	s_nop 0
	v_add_f32_e32 v93, 1.0, v93
	v_rcp_f32_e32 v93, v93
	s_nop 0
	v_mul_f32_e32 v88, v88, v93
	v_mul_f32_e32 v93, v88, v89
	v_mov_b32_e32 v88, v94
	v_mov_b32_e32 v89, v90
	v_pk_mul_f32 v[88:89], v[88:89], s[58:59] op_sel_hi:[1,0]
	s_nop 0
	v_mul_f32_e32 v90, 0xbfb8aa3b, v88
	v_exp_f32_e32 v90, v90
	s_nop 0
	v_add_f32_e32 v90, 1.0, v90
	v_rcp_f32_e32 v90, v90
	s_nop 0
	v_mul_f32_e32 v88, v88, v90
	v_mov_b32_e32 v90, v95
	v_mul_f32_e32 v94, v88, v89
	v_pk_mul_f32 v[88:89], v[90:91], s[58:59] op_sel_hi:[1,0]
	s_nop 0
	v_mul_f32_e32 v90, 0xbfb8aa3b, v88
	v_exp_f32_e32 v90, v90
	s_nop 0
	v_add_f32_e32 v90, 1.0, v90
	v_rcp_f32_e32 v90, v90
	s_nop 0
	v_mul_f32_e32 v88, v88, v90
	v_mul_f32_e32 v90, v88, v89
	v_mov_b32_e32 v88, v84
	v_mov_b32_e32 v89, v80
	v_pk_mul_f32 v[88:89], v[88:89], s[58:59] op_sel_hi:[1,0]
	s_nop 0
	v_mul_f32_e32 v80, 0xbfb8aa3b, v88
	v_exp_f32_e32 v80, v80
	s_nop 0
	v_add_f32_e32 v80, 1.0, v80
	v_rcp_f32_e32 v80, v80
	s_nop 0
	v_mul_f32_e32 v80, v88, v80
	v_mul_f32_e32 v84, v80, v89
	v_mov_b32_e32 v80, v85
	v_pk_mul_f32 v[80:81], v[80:81], s[58:59] op_sel_hi:[1,0]
	s_nop 0
	v_mul_f32_e32 v85, 0xbfb8aa3b, v80
	v_exp_f32_e32 v85, v85
	s_nop 0
	v_add_f32_e32 v85, 1.0, v85
	v_rcp_f32_e32 v85, v85
	s_nop 0
	v_mul_f32_e32 v80, v80, v85
	v_mul_f32_e32 v85, v80, v81
	v_mov_b32_e32 v80, v86
	v_mov_b32_e32 v81, v82
	v_pk_mul_f32 v[80:81], v[80:81], s[58:59] op_sel_hi:[1,0]
	s_nop 0
	v_mul_f32_e32 v82, 0xbfb8aa3b, v80
	v_exp_f32_e32 v82, v82
	s_nop 0
	v_add_f32_e32 v82, 1.0, v82
	v_rcp_f32_e32 v82, v82
	s_nop 0
	v_mul_f32_e32 v80, v80, v82
	v_mov_b32_e32 v82, v87
	v_mul_f32_e32 v86, v80, v81
	v_pk_mul_f32 v[80:81], v[82:83], s[58:59] op_sel_hi:[1,0]
	s_nop 0
	v_mul_f32_e32 v82, 0xbfb8aa3b, v80
	v_exp_f32_e32 v82, v82
	s_nop 0
	v_add_f32_e32 v82, 1.0, v82
	v_rcp_f32_e32 v82, v82
	s_nop 0
	v_mul_f32_e32 v80, v80, v82
	v_mul_f32_e32 v82, v80, v81
	v_mov_b32_e32 v80, v97
	v_mov_b32_e32 v81, v97
	v_cvt_pk_fp8_f32 v80, v92, v93
	v_cvt_pk_fp8_f32 v81, v84, v85
	v_cvt_pk_fp8_f32 v80, v94, v90 op_sel:[0,0,1]
	v_cvt_pk_fp8_f32 v81, v86, v82 op_sel:[0,0,1]
	v_or_b32_e32 v82, 32, v96
	v_mad_i64_i32 v[82:83], s[12:13], v82, s72, v[114:115]
	v_lshl_add_u64 v[82:83], v[82:83], 0, v[130:131]
	global_store_dwordx2 v[82:83], v[80:81], off
	v_mov_b32_e32 v80, v76
	v_mov_b32_e32 v81, v72
	v_pk_mul_f32 v[80:81], v[80:81], s[58:59] op_sel_hi:[1,0]
	s_nop 0
	v_mul_f32_e32 v72, 0xbfb8aa3b, v80
	v_exp_f32_e32 v72, v72
	s_nop 0
	v_add_f32_e32 v72, 1.0, v72
	v_rcp_f32_e32 v72, v72
	s_nop 0
	v_mul_f32_e32 v72, v80, v72
	v_mul_f32_e32 v76, v72, v81
	v_mov_b32_e32 v72, v77
	v_pk_mul_f32 v[72:73], v[72:73], s[58:59] op_sel_hi:[1,0]
	s_nop 0
	v_mul_f32_e32 v77, 0xbfb8aa3b, v72
	v_exp_f32_e32 v77, v77
	s_nop 0
	v_add_f32_e32 v77, 1.0, v77
	v_rcp_f32_e32 v77, v77
	s_nop 0
	v_mul_f32_e32 v72, v72, v77
	v_mul_f32_e32 v77, v72, v73
	v_mov_b32_e32 v72, v78
	v_mov_b32_e32 v73, v74
	v_pk_mul_f32 v[72:73], v[72:73], s[58:59] op_sel_hi:[1,0]
	s_nop 0
	v_mul_f32_e32 v74, 0xbfb8aa3b, v72
	v_exp_f32_e32 v74, v74
	s_nop 0
	v_add_f32_e32 v74, 1.0, v74
	v_rcp_f32_e32 v74, v74
	s_nop 0
	v_mul_f32_e32 v72, v72, v74
	v_mov_b32_e32 v74, v79
	v_mul_f32_e32 v78, v72, v73
	v_pk_mul_f32 v[72:73], v[74:75], s[58:59] op_sel_hi:[1,0]
	s_nop 0
	v_mul_f32_e32 v74, 0xbfb8aa3b, v72
	v_exp_f32_e32 v74, v74
	s_nop 0
	v_add_f32_e32 v74, 1.0, v74
	v_rcp_f32_e32 v74, v74
	s_nop 0
	v_mul_f32_e32 v72, v72, v74
	v_mul_f32_e32 v74, v72, v73
	v_mov_b32_e32 v72, v68
	v_mov_b32_e32 v73, v64
	v_pk_mul_f32 v[72:73], v[72:73], s[58:59] op_sel_hi:[1,0]
	s_nop 0
	v_mul_f32_e32 v64, 0xbfb8aa3b, v72
	v_exp_f32_e32 v64, v64
	s_nop 0
	v_add_f32_e32 v64, 1.0, v64
	v_rcp_f32_e32 v64, v64
	s_nop 0
	v_mul_f32_e32 v64, v72, v64
	v_mul_f32_e32 v68, v64, v73
	v_mov_b32_e32 v64, v69
	v_pk_mul_f32 v[64:65], v[64:65], s[58:59] op_sel_hi:[1,0]
	s_nop 0
	v_mul_f32_e32 v69, 0xbfb8aa3b, v64
	v_exp_f32_e32 v69, v69
	s_nop 0
	v_add_f32_e32 v69, 1.0, v69
	v_rcp_f32_e32 v69, v69
	s_nop 0
	v_mul_f32_e32 v64, v64, v69
	v_mul_f32_e32 v69, v64, v65
	v_mov_b32_e32 v64, v70
	v_mov_b32_e32 v65, v66
	v_pk_mul_f32 v[64:65], v[64:65], s[58:59] op_sel_hi:[1,0]
	s_nop 0
	v_mul_f32_e32 v66, 0xbfb8aa3b, v64
	v_exp_f32_e32 v66, v66
	s_nop 0
	v_add_f32_e32 v66, 1.0, v66
	v_rcp_f32_e32 v66, v66
	s_nop 0
	v_mul_f32_e32 v64, v64, v66
	v_mov_b32_e32 v66, v71
	v_mul_f32_e32 v70, v64, v65
	v_pk_mul_f32 v[64:65], v[66:67], s[58:59] op_sel_hi:[1,0]
	s_nop 0
	v_mul_f32_e32 v66, 0xbfb8aa3b, v64
	v_exp_f32_e32 v66, v66
	s_nop 0
	v_add_f32_e32 v66, 1.0, v66
	v_rcp_f32_e32 v66, v66
	s_nop 0
	v_mul_f32_e32 v64, v64, v66
	v_mul_f32_e32 v66, v64, v65
	v_mov_b32_e32 v64, v97
	v_mov_b32_e32 v65, v97
	v_cvt_pk_fp8_f32 v64, v76, v77
	v_cvt_pk_fp8_f32 v65, v68, v69
	v_cvt_pk_fp8_f32 v64, v78, v74 op_sel:[0,0,1]
	v_cvt_pk_fp8_f32 v65, v70, v66 op_sel:[0,0,1]
	v_or_b32_e32 v66, 48, v96
	v_mad_i64_i32 v[66:67], s[12:13], v66, s72, v[114:115]
	v_lshl_add_u64 v[66:67], v[66:67], 0, v[130:131]
	global_store_dwordx2 v[66:67], v[64:65], off
	v_mov_b32_e32 v64, v60
	v_mov_b32_e32 v65, v56
	v_pk_mul_f32 v[64:65], v[64:65], s[58:59] op_sel_hi:[1,0]
	v_add_u32_e32 v66, 0x80, v96
	v_mul_f32_e32 v56, 0xbfb8aa3b, v64
	v_exp_f32_e32 v56, v56
	s_nop 0
	v_add_f32_e32 v56, 1.0, v56
	v_rcp_f32_e32 v56, v56
	s_nop 0
	v_mul_f32_e32 v56, v64, v56
	v_mul_f32_e32 v60, v56, v65
	v_mov_b32_e32 v56, v61
	v_pk_mul_f32 v[56:57], v[56:57], s[58:59] op_sel_hi:[1,0]
	s_nop 0
	v_mul_f32_e32 v61, 0xbfb8aa3b, v56
	v_exp_f32_e32 v61, v61
	s_nop 0
	v_add_f32_e32 v61, 1.0, v61
	v_rcp_f32_e32 v61, v61
	s_nop 0
	v_mul_f32_e32 v56, v56, v61
	v_mul_f32_e32 v61, v56, v57
	v_mov_b32_e32 v56, v62
	v_mov_b32_e32 v57, v58
	v_pk_mul_f32 v[56:57], v[56:57], s[58:59] op_sel_hi:[1,0]
	s_nop 0
	v_mul_f32_e32 v58, 0xbfb8aa3b, v56
	v_exp_f32_e32 v58, v58
	s_nop 0
	v_add_f32_e32 v58, 1.0, v58
	v_rcp_f32_e32 v58, v58
	s_nop 0
	v_mul_f32_e32 v56, v56, v58
	v_mov_b32_e32 v58, v63
	v_mul_f32_e32 v62, v56, v57
	v_pk_mul_f32 v[56:57], v[58:59], s[58:59] op_sel_hi:[1,0]
	s_nop 0
	v_mul_f32_e32 v58, 0xbfb8aa3b, v56
	v_exp_f32_e32 v58, v58
	s_nop 0
	v_add_f32_e32 v58, 1.0, v58
	v_rcp_f32_e32 v58, v58
	s_nop 0
	v_mul_f32_e32 v56, v56, v58
	v_mul_f32_e32 v58, v56, v57
	v_mov_b32_e32 v56, v52
	v_mov_b32_e32 v57, v48
	v_pk_mul_f32 v[56:57], v[56:57], s[58:59] op_sel_hi:[1,0]
	s_nop 0
	v_mul_f32_e32 v48, 0xbfb8aa3b, v56
	v_exp_f32_e32 v48, v48
	s_nop 0
	v_add_f32_e32 v48, 1.0, v48
	v_rcp_f32_e32 v48, v48
	s_nop 0
	v_mul_f32_e32 v48, v56, v48
	v_mul_f32_e32 v52, v48, v57
	v_mov_b32_e32 v48, v53
	v_pk_mul_f32 v[48:49], v[48:49], s[58:59] op_sel_hi:[1,0]
	s_nop 0
	v_mul_f32_e32 v53, 0xbfb8aa3b, v48
	v_exp_f32_e32 v53, v53
	s_nop 0
	v_add_f32_e32 v53, 1.0, v53
	v_rcp_f32_e32 v53, v53
	s_nop 0
	v_mul_f32_e32 v48, v48, v53
	v_mul_f32_e32 v53, v48, v49
	v_mov_b32_e32 v48, v54
	v_mov_b32_e32 v49, v50
	v_pk_mul_f32 v[48:49], v[48:49], s[58:59] op_sel_hi:[1,0]
	s_nop 0
	v_mul_f32_e32 v50, 0xbfb8aa3b, v48
	v_exp_f32_e32 v50, v50
	s_nop 0
	v_add_f32_e32 v50, 1.0, v50
	v_rcp_f32_e32 v50, v50
	s_nop 0
	v_mul_f32_e32 v48, v48, v50
	v_mov_b32_e32 v50, v55
	v_mul_f32_e32 v54, v48, v49
	v_pk_mul_f32 v[48:49], v[50:51], s[58:59] op_sel_hi:[1,0]
	s_nop 0
	v_mul_f32_e32 v50, 0xbfb8aa3b, v48
	v_exp_f32_e32 v50, v50
	s_nop 0
	v_add_f32_e32 v50, 1.0, v50
	v_rcp_f32_e32 v50, v50
	s_nop 0
	v_mul_f32_e32 v48, v48, v50
	v_mul_f32_e32 v50, v48, v49
	v_mov_b32_e32 v48, v97
	v_mov_b32_e32 v49, v97
	v_cvt_pk_fp8_f32 v48, v60, v61
	v_cvt_pk_fp8_f32 v49, v52, v53
	v_cvt_pk_fp8_f32 v48, v62, v58 op_sel:[0,0,1]
	v_cvt_pk_fp8_f32 v49, v54, v50 op_sel:[0,0,1]
	v_mad_i64_i32 v[50:51], s[12:13], v66, s72, v[114:115]
	v_lshl_add_u64 v[50:51], v[50:51], 0, v[130:131]
	global_store_dwordx2 v[50:51], v[48:49], off
	v_mov_b32_e32 v48, v44
	v_mov_b32_e32 v49, v40
	v_pk_mul_f32 v[48:49], v[48:49], s[58:59] op_sel_hi:[1,0]
	s_nop 0
	v_mul_f32_e32 v40, 0xbfb8aa3b, v48
	v_exp_f32_e32 v40, v40
	s_nop 0
	v_add_f32_e32 v40, 1.0, v40
	v_rcp_f32_e32 v40, v40
	s_nop 0
	v_mul_f32_e32 v40, v48, v40
	v_mul_f32_e32 v44, v40, v49
	v_mov_b32_e32 v40, v45
	v_pk_mul_f32 v[40:41], v[40:41], s[58:59] op_sel_hi:[1,0]
	s_nop 0
	v_mul_f32_e32 v45, 0xbfb8aa3b, v40
	v_exp_f32_e32 v45, v45
	s_nop 0
	v_add_f32_e32 v45, 1.0, v45
	v_rcp_f32_e32 v45, v45
	s_nop 0
	v_mul_f32_e32 v40, v40, v45
	v_mul_f32_e32 v45, v40, v41
	v_mov_b32_e32 v40, v46
	v_mov_b32_e32 v41, v42
	v_pk_mul_f32 v[40:41], v[40:41], s[58:59] op_sel_hi:[1,0]
	s_nop 0
	v_mul_f32_e32 v42, 0xbfb8aa3b, v40
	v_exp_f32_e32 v42, v42
	s_nop 0
	v_add_f32_e32 v42, 1.0, v42
	v_rcp_f32_e32 v42, v42
	s_nop 0
	v_mul_f32_e32 v40, v40, v42
	v_mov_b32_e32 v42, v47
	v_mul_f32_e32 v46, v40, v41
	v_pk_mul_f32 v[40:41], v[42:43], s[58:59] op_sel_hi:[1,0]
	s_nop 0
	v_mul_f32_e32 v42, 0xbfb8aa3b, v40
	v_exp_f32_e32 v42, v42
	s_nop 0
	v_add_f32_e32 v42, 1.0, v42
	v_rcp_f32_e32 v42, v42
	s_nop 0
	v_mul_f32_e32 v40, v40, v42
	v_mul_f32_e32 v42, v40, v41
	v_mov_b32_e32 v40, v36
	v_mov_b32_e32 v41, v32
	v_pk_mul_f32 v[40:41], v[40:41], s[58:59] op_sel_hi:[1,0]
	s_nop 0
	v_mul_f32_e32 v32, 0xbfb8aa3b, v40
	v_exp_f32_e32 v32, v32
	s_nop 0
	v_add_f32_e32 v32, 1.0, v32
	v_rcp_f32_e32 v32, v32
	s_nop 0
	v_mul_f32_e32 v32, v40, v32
	v_mul_f32_e32 v36, v32, v41
	v_mov_b32_e32 v32, v37
	v_pk_mul_f32 v[32:33], v[32:33], s[58:59] op_sel_hi:[1,0]
	s_nop 0
	v_mul_f32_e32 v37, 0xbfb8aa3b, v32
	v_exp_f32_e32 v37, v37
	s_nop 0
	v_add_f32_e32 v37, 1.0, v37
	v_rcp_f32_e32 v37, v37
	s_nop 0
	v_mul_f32_e32 v32, v32, v37
	v_mul_f32_e32 v37, v32, v33
	v_mov_b32_e32 v32, v38
	v_mov_b32_e32 v33, v34
	v_pk_mul_f32 v[32:33], v[32:33], s[58:59] op_sel_hi:[1,0]
	s_nop 0
	v_mul_f32_e32 v34, 0xbfb8aa3b, v32
	v_exp_f32_e32 v34, v34
	s_nop 0
	v_add_f32_e32 v34, 1.0, v34
	v_rcp_f32_e32 v34, v34
	s_nop 0
	v_mul_f32_e32 v32, v32, v34
	v_mov_b32_e32 v34, v39
	v_mul_f32_e32 v38, v32, v33
	v_pk_mul_f32 v[32:33], v[34:35], s[58:59] op_sel_hi:[1,0]
	s_nop 0
	v_mul_f32_e32 v34, 0xbfb8aa3b, v32
	v_exp_f32_e32 v34, v34
	s_nop 0
	v_add_f32_e32 v34, 1.0, v34
	v_rcp_f32_e32 v34, v34
	s_nop 0
	v_mul_f32_e32 v32, v32, v34
	v_mul_f32_e32 v34, v32, v33
	v_mov_b32_e32 v32, v97
	v_mov_b32_e32 v33, v97
	v_cvt_pk_fp8_f32 v32, v44, v45
	v_cvt_pk_fp8_f32 v33, v36, v37
	v_cvt_pk_fp8_f32 v32, v46, v42 op_sel:[0,0,1]
	v_cvt_pk_fp8_f32 v33, v38, v34 op_sel:[0,0,1]
	v_add_u32_e32 v34, 0x90, v96
	v_mad_i64_i32 v[34:35], s[12:13], v34, s72, v[114:115]
	v_lshl_add_u64 v[34:35], v[34:35], 0, v[130:131]
	global_store_dwordx2 v[34:35], v[32:33], off
	v_mov_b32_e32 v32, v28
	v_mov_b32_e32 v33, v24
	v_pk_mul_f32 v[32:33], v[32:33], s[58:59] op_sel_hi:[1,0]
	s_nop 0
	v_mul_f32_e32 v24, 0xbfb8aa3b, v32
	v_exp_f32_e32 v24, v24
	s_nop 0
	v_add_f32_e32 v24, 1.0, v24
	v_rcp_f32_e32 v24, v24
	s_nop 0
	v_mul_f32_e32 v24, v32, v24
	v_mul_f32_e32 v28, v24, v33
	v_mov_b32_e32 v24, v29
	v_pk_mul_f32 v[24:25], v[24:25], s[58:59] op_sel_hi:[1,0]
	s_nop 0
	v_mul_f32_e32 v29, 0xbfb8aa3b, v24
	v_exp_f32_e32 v29, v29
	s_nop 0
	v_add_f32_e32 v29, 1.0, v29
	v_rcp_f32_e32 v29, v29
	s_nop 0
	v_mul_f32_e32 v24, v24, v29
	v_mul_f32_e32 v29, v24, v25
	v_mov_b32_e32 v24, v30
	v_mov_b32_e32 v25, v26
	v_pk_mul_f32 v[24:25], v[24:25], s[58:59] op_sel_hi:[1,0]
	s_nop 0
	v_mul_f32_e32 v26, 0xbfb8aa3b, v24
	v_exp_f32_e32 v26, v26
	s_nop 0
	v_add_f32_e32 v26, 1.0, v26
	v_rcp_f32_e32 v26, v26
	s_nop 0
	v_mul_f32_e32 v24, v24, v26
	v_mov_b32_e32 v26, v31
	v_mul_f32_e32 v30, v24, v25
	v_pk_mul_f32 v[24:25], v[26:27], s[58:59] op_sel_hi:[1,0]
	s_nop 0
	v_mul_f32_e32 v26, 0xbfb8aa3b, v24
	v_exp_f32_e32 v26, v26
	s_nop 0
	v_add_f32_e32 v26, 1.0, v26
	v_rcp_f32_e32 v26, v26
	s_nop 0
	v_mul_f32_e32 v24, v24, v26
	v_mul_f32_e32 v26, v24, v25
	v_mov_b32_e32 v24, v20
	v_mov_b32_e32 v25, v16
	v_pk_mul_f32 v[24:25], v[24:25], s[58:59] op_sel_hi:[1,0]
	s_nop 0
	v_mul_f32_e32 v16, 0xbfb8aa3b, v24
	v_exp_f32_e32 v16, v16
	s_nop 0
	v_add_f32_e32 v16, 1.0, v16
	v_rcp_f32_e32 v16, v16
	s_nop 0
	v_mul_f32_e32 v16, v24, v16
	v_mul_f32_e32 v20, v16, v25
	v_mov_b32_e32 v16, v21
	v_pk_mul_f32 v[16:17], v[16:17], s[58:59] op_sel_hi:[1,0]
	s_nop 0
	v_mul_f32_e32 v21, 0xbfb8aa3b, v16
	v_exp_f32_e32 v21, v21
	s_nop 0
	v_add_f32_e32 v21, 1.0, v21
	v_rcp_f32_e32 v21, v21
	s_nop 0
	v_mul_f32_e32 v16, v16, v21
	v_mul_f32_e32 v21, v16, v17
	v_mov_b32_e32 v16, v22
	v_mov_b32_e32 v17, v18
	v_pk_mul_f32 v[16:17], v[16:17], s[58:59] op_sel_hi:[1,0]
	s_nop 0
	v_mul_f32_e32 v18, 0xbfb8aa3b, v16
	v_exp_f32_e32 v18, v18
	s_nop 0
	v_add_f32_e32 v18, 1.0, v18
	v_rcp_f32_e32 v18, v18
	s_nop 0
	v_mul_f32_e32 v16, v16, v18
	v_mov_b32_e32 v18, v23
	v_mul_f32_e32 v22, v16, v17
	v_pk_mul_f32 v[16:17], v[18:19], s[58:59] op_sel_hi:[1,0]
	s_nop 0
	v_mul_f32_e32 v18, 0xbfb8aa3b, v16
	v_exp_f32_e32 v18, v18
	s_nop 0
	v_add_f32_e32 v18, 1.0, v18
	v_rcp_f32_e32 v18, v18
	s_nop 0
	v_mul_f32_e32 v16, v16, v18
	v_mul_f32_e32 v18, v16, v17
	v_mov_b32_e32 v16, v97
	v_mov_b32_e32 v17, v97
	v_cvt_pk_fp8_f32 v16, v28, v29
	v_cvt_pk_fp8_f32 v17, v20, v21
	v_cvt_pk_fp8_f32 v16, v30, v26 op_sel:[0,0,1]
	v_cvt_pk_fp8_f32 v17, v22, v18 op_sel:[0,0,1]
	v_add_u32_e32 v18, 0xa0, v96
	v_mad_i64_i32 v[18:19], s[12:13], v18, s72, v[114:115]
	v_lshl_add_u64 v[18:19], v[18:19], 0, v[130:131]
	global_store_dwordx2 v[18:19], v[16:17], off
	v_mov_b32_e32 v16, v12
	v_mov_b32_e32 v17, v8
	v_pk_mul_f32 v[16:17], v[16:17], s[58:59] op_sel_hi:[1,0]
	s_nop 0
	v_mul_f32_e32 v8, 0xbfb8aa3b, v16
	v_exp_f32_e32 v8, v8
	s_nop 0
	v_add_f32_e32 v8, 1.0, v8
	v_rcp_f32_e32 v8, v8
	s_nop 0
	v_mul_f32_e32 v8, v16, v8
	v_mul_f32_e32 v12, v8, v17
	v_mov_b32_e32 v8, v13
	v_pk_mul_f32 v[8:9], v[8:9], s[58:59] op_sel_hi:[1,0]
	s_nop 0
	v_mul_f32_e32 v13, 0xbfb8aa3b, v8
	v_exp_f32_e32 v13, v13
	s_nop 0
	v_add_f32_e32 v13, 1.0, v13
	v_rcp_f32_e32 v13, v13
	s_nop 0
	v_mul_f32_e32 v8, v8, v13
	v_mul_f32_e32 v13, v8, v9
	v_mov_b32_e32 v8, v14
	v_mov_b32_e32 v9, v10
	v_pk_mul_f32 v[8:9], v[8:9], s[58:59] op_sel_hi:[1,0]
	s_nop 0
	v_mul_f32_e32 v10, 0xbfb8aa3b, v8
	v_exp_f32_e32 v10, v10
	s_nop 0
	v_add_f32_e32 v10, 1.0, v10
	v_rcp_f32_e32 v10, v10
	s_nop 0
	v_mul_f32_e32 v8, v8, v10
	v_mov_b32_e32 v10, v15
	v_mul_f32_e32 v14, v8, v9
	v_pk_mul_f32 v[8:9], v[10:11], s[58:59] op_sel_hi:[1,0]
	s_nop 0
	v_mul_f32_e32 v10, 0xbfb8aa3b, v8
	v_exp_f32_e32 v10, v10
	s_nop 0
	v_add_f32_e32 v10, 1.0, v10
	v_rcp_f32_e32 v10, v10
	s_nop 0
	v_mul_f32_e32 v8, v8, v10
	v_mul_f32_e32 v10, v8, v9
	v_mov_b32_e32 v8, v4
	v_mov_b32_e32 v9, v0
	v_pk_mul_f32 v[8:9], v[8:9], s[58:59] op_sel_hi:[1,0]
	s_nop 0
	v_mul_f32_e32 v0, 0xbfb8aa3b, v8
	v_exp_f32_e32 v0, v0
	s_nop 0
	v_add_f32_e32 v0, 1.0, v0
	v_rcp_f32_e32 v0, v0
	s_nop 0
	v_mul_f32_e32 v0, v8, v0
	v_mul_f32_e32 v4, v0, v9
	v_mov_b32_e32 v0, v5
	v_pk_mul_f32 v[0:1], v[0:1], s[58:59] op_sel_hi:[1,0]
	s_nop 0
	v_mul_f32_e32 v5, 0xbfb8aa3b, v0
	v_exp_f32_e32 v5, v5
	s_nop 0
	v_add_f32_e32 v5, 1.0, v5
	v_rcp_f32_e32 v5, v5
	s_nop 0
	v_mul_f32_e32 v0, v0, v5
	v_mul_f32_e32 v5, v0, v1
	v_mov_b32_e32 v0, v6
	v_mov_b32_e32 v1, v2
	v_pk_mul_f32 v[0:1], v[0:1], s[58:59] op_sel_hi:[1,0]
	s_nop 0
	v_mul_f32_e32 v2, 0xbfb8aa3b, v0
	v_exp_f32_e32 v2, v2
	s_nop 0
	v_add_f32_e32 v2, 1.0, v2
	v_rcp_f32_e32 v2, v2
	s_nop 0
	v_mul_f32_e32 v0, v0, v2
	v_mov_b32_e32 v2, v7
	v_mul_f32_e32 v6, v0, v1
	v_pk_mul_f32 v[0:1], v[2:3], s[58:59] op_sel_hi:[1,0]
	s_nop 0
	v_mul_f32_e32 v2, 0xbfb8aa3b, v0
	v_exp_f32_e32 v2, v2
	s_nop 0
	v_add_f32_e32 v2, 1.0, v2
	v_rcp_f32_e32 v2, v2
	s_nop 0
	v_mul_f32_e32 v0, v0, v2
	v_mul_f32_e32 v2, v0, v1
	v_mov_b32_e32 v0, v97
	v_mov_b32_e32 v1, v97
	v_cvt_pk_fp8_f32 v0, v12, v13
	v_cvt_pk_fp8_f32 v1, v4, v5
	v_cvt_pk_fp8_f32 v0, v14, v10 op_sel:[0,0,1]
	v_cvt_pk_fp8_f32 v1, v6, v2 op_sel:[0,0,1]
	v_add_u32_e32 v2, 0xb0, v96
	v_mad_i64_i32 v[2:3], s[12:13], v2, s72, v[114:115]
	v_lshl_add_u64 v[2:3], v[2:3], 0, v[130:131]
	s_mov_b64 s[12:13], -1
	global_store_dwordx2 v[2:3], v[0:1], off
	s_cbranch_scc1 .LBB0_2125
	s_andn2_b64 vcc, exec, s[2:3]
	s_branch .LBB0_2124
